# plus: in every GEMM phase the 8 B-fragment LDS reads are issued before the phase's DMA address/m0 setup
# baseline (speedup 1.0000x reference)
; #define PG8_AOFF(of, u) do { _Pragma("unroll") for (int hh_ = 0; hh_ < 2; ++hh_) _Pragma("unroll") for (int i_ = 0; i_ < 2; ++i_) { \
;         if constexpr (GATHER) of[hh_][i_] = (unsigned)gidx[(u).pm * 256 + hh_ * 128 + RA[i_]] * (unsigned)(lda * 2) + CA2[i_]; \
;         else of[hh_][i_] = (unsigned)((hh_ * HALF + RA[i_]) * lda) * 2u + CA2[i_]; } } while (0)
; #define PG8_STAGE(bufoff, gbase, voff) do { _Pragma("unroll") for (int _i = 0; _i < 2; ++_i) \
;         __builtin_amdgcn_global_load_lds((const unsigned*)((const char*)(gbase) + (voff)[_i]), (LAS unsigned*)(lds + (bufoff) + ldsw + _i * 8192), 16, 0, 0); } while (0)
; #define PG8_LDA(dst, b, h) do { _Pragma("unroll") for (int m = 0; m < 4; ++m) _Pragma("unroll") for (int k = 0; k < 2; ++k) dst[m][k] = *(const LAS bf16x8*)(lds + PG8_SA(b, h) + aoff + m * 2048 + k * 1024); } while (0)
; #define PG8_WAIT_V(n) asm volatile("s_waitcnt vmcnt(" #n ")" ::: "memory")
; #define PG8_WAIT_L(n) asm volatile("s_waitcnt lgkmcnt(" #n ")" ::: "memory")
; template <class Epi, class Sched, bool GATHER = false>
; __device__ __forceinline__ void gemm_phase(LAS unsigned char* lds, const int lda, const int ldb, const int K, const Sched& S, const Epi& E, const int* gidx = nullptr) {
;     ...
;             const bool last = (t == nt - 2);
;             if constexpr (GATHER) { if (last && has_next) PG8_AOFF(ofn, nxt); }
;             const char* a1 = cA + (size_t)(t + 1) * kstep;
;             const char* a2 = last ? nA : cA + (size_t)(t + 2) * kstep; const char* b2 = last ? nB : cB + (size_t)(t + 2) * kstep;
;             const char* a3 = a2 + kstep; const char* b3 = b2 + kstep;
;             unsigned o2[2][2];
; #pragma unroll
;             for (int hh = 0; hh < 2; ++hh)
; #pragma unroll
;                 for (int i = 0; i < 2; ++i) { if constexpr (GATHER) o2[hh][i] = last ? ofn[hh][i] : ofc[hh][i]; else o2[hh][i] = ofc[hh][i]; }
;             PG8_LDB(B0, 0, 0); PG8_LDB(B1, 0, 1); PG8_SCHED; PG8_LDA(At, 0, 0); PG8_STAGE(PG8_SA(1, 1), a1, ofc[1]);
;             PG8_WAIT_V(8); PG8_WAIT_L(0); PG8_BAR; PG8_MMA(0, 0, At, B0); PG8_MMA(0, 1, At, B1); PG8_BAR; PG8_SCHED;
;             PG8_LDA(At, 0, 1); PG8_STAGE(PG8_SB(0, 0), b2, voffB); PG8_STAGE(PG8_SB(0, 1), b2 + hstepB, voffB); PG8_STAGE(PG8_SA(0, 0), a2, o2[0]);
;             PG8_WAIT_V(8); PG8_WAIT_L(0); PG8_BAR; PG8_MMA(1, 0, At, B0); PG8_MMA(1, 1, At, B1); PG8_BAR; PG8_SCHED;
.LBB0_428:
	s_add_i32 s28, 0, 0x10000
	s_add_i32 s33, 0, 0x14000
	v_add_u32_e32 v142, s28, v175
	v_add_u32_e32 v158, s33, v175
	ds_read_b128 v[126:129], v142
	ds_read_b128 v[130:133], v142 offset:1024
	ds_read_b128 v[138:141], v142 offset:2048
	ds_read_b128 v[142:145], v142 offset:3072
	ds_read_b128 v[146:149], v158
	ds_read_b128 v[150:153], v158 offset:1024
	ds_read_b128 v[154:157], v158 offset:2048
	ds_read_b128 v[158:161], v158 offset:3072
	ds_read_b128 v[182:185], v229
	ds_read_b128 v[186:189], v229 offset:1024
	ds_read_b128 v[190:193], v229 offset:2048
	ds_read_b128 v[196:199], v229 offset:3072
	ds_read_b128 v[200:203], v229 offset:4096
	ds_read_b128 v[204:207], v229 offset:5120
	ds_read_b128 v[208:211], v229 offset:6144
	ds_read_b128 v[230:233], v229 offset:7168
	v_lshl_add_u64 v[234:235], s[72:73], 0, v[180:181]
	s_add_i32 m0, s59, 0xc000
	s_add_u32 s12, s72, 0x80
	s_addc_u32 s13, s73, 0
	s_cmp_eq_u32 s75, 28
	s_cselect_b32 s67, s81, s13
	s_cselect_b32 s66, s80, s12
	s_cselect_b32 s13, s83, s74
	s_cselect_b32 s12, s82, s60
	global_load_lds_dwordx4 v[234:235], off
	v_lshl_add_u64 v[234:235], s[72:73], 0, v[178:179]
	s_add_i32 m0, s59, 0xe000
	s_nop 0
	global_load_lds_dwordx4 v[234:235], off
	s_waitcnt vmcnt(8)
	s_waitcnt lgkmcnt(0)
	s_barrier
	v_mfma_f32_16x16x32_bf16 v[134:137], v[126:129], v[182:185], v[134:137]
	v_mfma_f32_16x16x32_bf16 v[122:125], v[138:141], v[182:185], v[122:125]
	v_mfma_f32_16x16x32_bf16 v[110:113], v[126:129], v[190:193], v[110:113]
	v_mfma_f32_16x16x32_bf16 v[106:109], v[138:141], v[190:193], v[106:109]
	v_mfma_f32_16x16x32_bf16 v[94:97], v[126:129], v[200:203], v[94:97]
	v_mfma_f32_16x16x32_bf16 v[90:93], v[138:141], v[200:203], v[90:93]
	v_mfma_f32_16x16x32_bf16 v[78:81], v[126:129], v[208:211], v[78:81]
	v_mfma_f32_16x16x32_bf16 v[74:77], v[138:141], v[208:211], v[74:77]
	v_mfma_f32_16x16x32_bf16 v[134:137], v[130:133], v[186:189], v[134:137]
	v_mfma_f32_16x16x32_bf16 v[122:125], v[142:145], v[186:189], v[122:125]
	v_mfma_f32_16x16x32_bf16 v[110:113], v[130:133], v[196:199], v[110:113]
	v_mfma_f32_16x16x32_bf16 v[106:109], v[142:145], v[196:199], v[106:109]
	v_mfma_f32_16x16x32_bf16 v[94:97], v[130:133], v[204:207], v[94:97]
	v_mfma_f32_16x16x32_bf16 v[90:93], v[142:145], v[204:207], v[90:93]
	v_mfma_f32_16x16x32_bf16 v[78:81], v[130:133], v[230:233], v[78:81]
	v_mfma_f32_16x16x32_bf16 v[74:77], v[142:145], v[230:233], v[74:77]
	v_mfma_f32_16x16x32_bf16 v[118:121], v[146:149], v[182:185], v[118:121]
	v_mfma_f32_16x16x32_bf16 v[114:117], v[154:157], v[182:185], v[114:117]
	v_mfma_f32_16x16x32_bf16 v[102:105], v[146:149], v[190:193], v[102:105]
	v_mfma_f32_16x16x32_bf16 v[98:101], v[154:157], v[190:193], v[98:101]
	v_mfma_f32_16x16x32_bf16 v[86:89], v[146:149], v[200:203], v[86:89]
	v_mfma_f32_16x16x32_bf16 v[82:85], v[154:157], v[200:203], v[82:85]
	v_mfma_f32_16x16x32_bf16 v[70:73], v[146:149], v[208:211], v[70:73]
	v_mfma_f32_16x16x32_bf16 v[66:69], v[154:157], v[208:211], v[66:69]
	v_mfma_f32_16x16x32_bf16 v[118:121], v[150:153], v[186:189], v[118:121]
	v_mfma_f32_16x16x32_bf16 v[114:117], v[158:161], v[186:189], v[114:117]
	v_mfma_f32_16x16x32_bf16 v[102:105], v[150:153], v[196:199], v[102:105]
	v_mfma_f32_16x16x32_bf16 v[98:101], v[158:161], v[196:199], v[98:101]
	v_mfma_f32_16x16x32_bf16 v[86:89], v[150:153], v[204:207], v[86:89]
	v_mfma_f32_16x16x32_bf16 v[82:85], v[158:161], v[204:207], v[82:85]
	v_mfma_f32_16x16x32_bf16 v[70:73], v[150:153], v[230:233], v[70:73]
	v_mfma_f32_16x16x32_bf16 v[66:69], v[158:161], v[230:233], v[66:69]
	s_barrier
	ds_read_b128 v[182:185], v229 offset:16384
	ds_read_b128 v[186:189], v229 offset:17408
	ds_read_b128 v[190:193], v229 offset:18432
	ds_read_b128 v[196:199], v229 offset:19456
	ds_read_b128 v[200:203], v229 offset:20480
	ds_read_b128 v[204:207], v229 offset:21504
	ds_read_b128 v[208:211], v229 offset:22528
	ds_read_b128 v[230:233], v229 offset:23552
	s_add_i32 s28, s28, s43
	v_lshl_add_u64 v[234:235], s[12:13], 0, v[162:163]
	s_mov_b32 m0, s28
	s_nop 0
	global_load_lds_dwordx4 v[234:235], off
	s_add_i32 m0, s28, 0x2000
	s_add_u32 s28, s12, 0x80000
	v_lshl_add_u64 v[236:237], s[12:13], 0, v[164:165]
	s_addc_u32 s29, s13, 0
	s_add_i32 s33, s33, s43
	global_load_lds_dwordx4 v[236:237], off
	v_lshl_add_u64 v[238:239], s[28:29], 0, v[162:163]
	s_mov_b32 m0, s33
	v_lshl_add_u64 v[240:241], s[66:67], 0, v[168:169]
	global_load_lds_dwordx4 v[238:239], off
	v_lshl_add_u64 v[238:239], s[28:29], 0, v[164:165]
	s_add_i32 m0, s33, 0x2000
	s_nop 0
	global_load_lds_dwordx4 v[238:239], off
	v_lshl_add_u64 v[238:239], s[66:67], 0, v[166:167]
	s_mov_b32 m0, s59
	s_nop 0
	global_load_lds_dwordx4 v[238:239], off
	s_mov_b32 m0, s36
	s_nop 0
	global_load_lds_dwordx4 v[240:241], off
	s_waitcnt vmcnt(8)
	s_waitcnt lgkmcnt(0)
	s_barrier
; #define PG8_STAGE(bufoff, gbase, voff) do { _Pragma("unroll") for (int _i = 0; _i < 2; ++_i) \
;         __builtin_amdgcn_global_load_lds((const unsigned*)((const char*)(gbase) + (voff)[_i]), (LAS unsigned*)(lds + (bufoff) + ldsw + _i * 8192), 16, 0, 0); } while (0)
; #define PG8_LDA(dst, b, h) do { _Pragma("unroll") for (int m = 0; m < 4; ++m) _Pragma("unroll") for (int k = 0; k < 2; ++k) dst[m][k] = *(const LAS bf16x8*)(lds + PG8_SA(b, h) + aoff + m * 2048 + k * 1024); } while (0)
; #define PG8_LDB(dst, b, h) do { _Pragma("unroll") for (int n = 0; n < 2; ++n) _Pragma("unroll") for (int k = 0; k < 2; ++k) dst[n][k] = *(const LAS bf16x8*)(lds + PG8_SB(b, h) + boff + n * 2048 + k * 1024); } while (0)
; #define PG8_MMA(ai, bj, At, Bt) do { __builtin_amdgcn_s_setprio(1); _Pragma("unroll") for (int m = 0; m < 4; ++m) _Pragma("unroll") for (int n = 0; n < 2; ++n) _Pragma("unroll") for (int k = 0; k < 2; ++k) \
;         acc[ai][bj][m][n] = __builtin_amdgcn_mfma_f32_16x16x32_bf16(Bt[n][k], At[m][k], acc[ai][bj][m][n], 0, 0, 0); __builtin_amdgcn_s_setprio(0); } while (0)
; #define PG8_WAIT_V(n) asm volatile("s_waitcnt vmcnt(" #n ")" ::: "memory")
; #define PG8_WAIT_L(n) asm volatile("s_waitcnt lgkmcnt(" #n ")" ::: "memory")
; #define PG8_BAR __builtin_amdgcn_s_barrier()
; #define PG8_SCHED __builtin_amdgcn_sched_barrier(0)
; template <class Epi, class Sched, bool GATHER = false>
; __device__ __forceinline__ void gemm_phase(LAS unsigned char* lds, const int lda, const int ldb, const int K, const Sched& S, const Epi& E, const int* gidx = nullptr) {
;     ...
;             PG8_WAIT_V(8); PG8_WAIT_L(0); PG8_BAR; PG8_MMA(1, 0, At, B0); PG8_MMA(1, 1, At, B1); PG8_BAR; PG8_SCHED;
;             PG8_LDB(B0, 1, 0); PG8_LDB(B1, 1, 1); PG8_SCHED; PG8_LDA(At, 1, 0); PG8_STAGE(PG8_SA(0, 1), a2, o2[1]);
;             PG8_WAIT_V(8); PG8_WAIT_L(0); PG8_BAR; PG8_MMA(0, 0, At, B0); PG8_MMA(0, 1, At, B1); PG8_BAR; PG8_SCHED;
	v_mfma_f32_16x16x32_bf16 v[62:65], v[126:129], v[182:185], v[62:65]
	v_mfma_f32_16x16x32_bf16 v[58:61], v[138:141], v[182:185], v[58:61]
	v_mfma_f32_16x16x32_bf16 v[46:49], v[126:129], v[190:193], v[46:49]
	v_mfma_f32_16x16x32_bf16 v[42:45], v[138:141], v[190:193], v[42:45]
	v_mfma_f32_16x16x32_bf16 v[30:33], v[126:129], v[200:203], v[30:33]
	v_mfma_f32_16x16x32_bf16 v[26:29], v[138:141], v[200:203], v[26:29]
	v_mfma_f32_16x16x32_bf16 v[14:17], v[126:129], v[208:211], v[14:17]
	v_mfma_f32_16x16x32_bf16 v[10:13], v[138:141], v[208:211], v[10:13]
	v_mfma_f32_16x16x32_bf16 v[62:65], v[130:133], v[186:189], v[62:65]
	v_mfma_f32_16x16x32_bf16 v[58:61], v[142:145], v[186:189], v[58:61]
	v_mfma_f32_16x16x32_bf16 v[46:49], v[130:133], v[196:199], v[46:49]
	v_mfma_f32_16x16x32_bf16 v[42:45], v[142:145], v[196:199], v[42:45]
	v_mfma_f32_16x16x32_bf16 v[30:33], v[130:133], v[204:207], v[30:33]
	v_mfma_f32_16x16x32_bf16 v[26:29], v[142:145], v[204:207], v[26:29]
	v_mfma_f32_16x16x32_bf16 v[14:17], v[130:133], v[230:233], v[14:17]
	v_mfma_f32_16x16x32_bf16 v[10:13], v[142:145], v[230:233], v[10:13]
	v_mfma_f32_16x16x32_bf16 v[54:57], v[146:149], v[182:185], v[54:57]
	v_mfma_f32_16x16x32_bf16 v[50:53], v[154:157], v[182:185], v[50:53]
	v_mfma_f32_16x16x32_bf16 v[38:41], v[146:149], v[190:193], v[38:41]
	v_mfma_f32_16x16x32_bf16 v[34:37], v[154:157], v[190:193], v[34:37]
	v_mfma_f32_16x16x32_bf16 v[22:25], v[146:149], v[200:203], v[22:25]
	v_mfma_f32_16x16x32_bf16 v[18:21], v[154:157], v[200:203], v[18:21]
	v_mfma_f32_16x16x32_bf16 v[6:9], v[146:149], v[208:211], v[6:9]
	v_mfma_f32_16x16x32_bf16 v[2:5], v[154:157], v[208:211], v[2:5]
	v_mfma_f32_16x16x32_bf16 v[54:57], v[150:153], v[186:189], v[54:57]
	v_mfma_f32_16x16x32_bf16 v[50:53], v[158:161], v[186:189], v[50:53]
	v_mfma_f32_16x16x32_bf16 v[38:41], v[150:153], v[196:199], v[38:41]
	v_mfma_f32_16x16x32_bf16 v[34:37], v[158:161], v[196:199], v[34:37]
	v_mfma_f32_16x16x32_bf16 v[22:25], v[150:153], v[204:207], v[22:25]
	v_mfma_f32_16x16x32_bf16 v[18:21], v[158:161], v[204:207], v[18:21]
	v_mfma_f32_16x16x32_bf16 v[6:9], v[150:153], v[230:233], v[6:9]
	v_mfma_f32_16x16x32_bf16 v[2:5], v[158:161], v[230:233], v[2:5]
	s_barrier
	s_add_i32 s28, 0, 0x18000
	s_add_i32 s29, 0, 0x1c000
	v_add_u32_e32 v142, s28, v175
	v_add_u32_e32 v158, s29, v175
	ds_read_b128 v[126:129], v142
	ds_read_b128 v[130:133], v142 offset:1024
	ds_read_b128 v[138:141], v142 offset:2048
	ds_read_b128 v[142:145], v142 offset:3072
	ds_read_b128 v[146:149], v158
	ds_read_b128 v[150:153], v158 offset:1024
	ds_read_b128 v[154:157], v158 offset:2048
	ds_read_b128 v[158:161], v158 offset:3072
	ds_read_b128 v[182:185], v229 offset:32768
	ds_read_b128 v[186:189], v229 offset:33792
	ds_read_b128 v[190:193], v229 offset:34816
	ds_read_b128 v[196:199], v229 offset:35840
	ds_read_b128 v[200:203], v229 offset:36864
	ds_read_b128 v[204:207], v229 offset:37888
	ds_read_b128 v[208:211], v229 offset:38912
	ds_read_b128 v[230:233], v229 offset:39936
	s_mov_b32 m0, s37
	v_lshl_add_u64 v[242:243], s[66:67], 0, v[170:171]
	global_load_lds_dwordx4 v[242:243], off
	v_lshl_add_u64 v[242:243], s[66:67], 0, v[172:173]
	s_mov_b32 m0, s22
	s_nop 0
	global_load_lds_dwordx4 v[242:243], off
	s_waitcnt vmcnt(8)
	s_waitcnt lgkmcnt(0)
	s_barrier
	v_mfma_f32_16x16x32_bf16 v[134:137], v[126:129], v[182:185], v[134:137]
	v_mfma_f32_16x16x32_bf16 v[122:125], v[138:141], v[182:185], v[122:125]
	v_mfma_f32_16x16x32_bf16 v[110:113], v[126:129], v[190:193], v[110:113]
	v_mfma_f32_16x16x32_bf16 v[106:109], v[138:141], v[190:193], v[106:109]
	v_mfma_f32_16x16x32_bf16 v[94:97], v[126:129], v[200:203], v[94:97]
	v_mfma_f32_16x16x32_bf16 v[90:93], v[138:141], v[200:203], v[90:93]
	v_mfma_f32_16x16x32_bf16 v[78:81], v[126:129], v[208:211], v[78:81]
	v_mfma_f32_16x16x32_bf16 v[74:77], v[138:141], v[208:211], v[74:77]
	v_mfma_f32_16x16x32_bf16 v[134:137], v[130:133], v[186:189], v[134:137]
	v_mfma_f32_16x16x32_bf16 v[122:125], v[142:145], v[186:189], v[122:125]
	v_mfma_f32_16x16x32_bf16 v[110:113], v[130:133], v[196:199], v[110:113]
	v_mfma_f32_16x16x32_bf16 v[106:109], v[142:145], v[196:199], v[106:109]
	v_mfma_f32_16x16x32_bf16 v[94:97], v[130:133], v[204:207], v[94:97]
	v_mfma_f32_16x16x32_bf16 v[90:93], v[142:145], v[204:207], v[90:93]
	v_mfma_f32_16x16x32_bf16 v[78:81], v[130:133], v[230:233], v[78:81]
	v_mfma_f32_16x16x32_bf16 v[74:77], v[142:145], v[230:233], v[74:77]
	v_mfma_f32_16x16x32_bf16 v[118:121], v[146:149], v[182:185], v[118:121]
	v_mfma_f32_16x16x32_bf16 v[114:117], v[154:157], v[182:185], v[114:117]
	v_mfma_f32_16x16x32_bf16 v[102:105], v[146:149], v[190:193], v[102:105]
	v_mfma_f32_16x16x32_bf16 v[98:101], v[154:157], v[190:193], v[98:101]
	v_mfma_f32_16x16x32_bf16 v[86:89], v[146:149], v[200:203], v[86:89]
	v_mfma_f32_16x16x32_bf16 v[82:85], v[154:157], v[200:203], v[82:85]
	v_mfma_f32_16x16x32_bf16 v[70:73], v[146:149], v[208:211], v[70:73]
	v_mfma_f32_16x16x32_bf16 v[66:69], v[154:157], v[208:211], v[66:69]
	v_mfma_f32_16x16x32_bf16 v[118:121], v[150:153], v[186:189], v[118:121]
	v_mfma_f32_16x16x32_bf16 v[114:117], v[158:161], v[186:189], v[114:117]
	v_mfma_f32_16x16x32_bf16 v[102:105], v[150:153], v[196:199], v[102:105]
	v_mfma_f32_16x16x32_bf16 v[98:101], v[158:161], v[196:199], v[98:101]
	v_mfma_f32_16x16x32_bf16 v[86:89], v[150:153], v[204:207], v[86:89]
	v_mfma_f32_16x16x32_bf16 v[82:85], v[158:161], v[204:207], v[82:85]
	v_mfma_f32_16x16x32_bf16 v[70:73], v[150:153], v[230:233], v[70:73]
	v_mfma_f32_16x16x32_bf16 v[66:69], v[158:161], v[230:233], v[66:69]
	s_barrier
; #define PG8_STAGE(bufoff, gbase, voff) do { _Pragma("unroll") for (int _i = 0; _i < 2; ++_i) \
;         __builtin_amdgcn_global_load_lds((const unsigned*)((const char*)(gbase) + (voff)[_i]), (LAS unsigned*)(lds + (bufoff) + ldsw + _i * 8192), 16, 0, 0); } while (0)
; #define PG8_LDA(dst, b, h) do { _Pragma("unroll") for (int m = 0; m < 4; ++m) _Pragma("unroll") for (int k = 0; k < 2; ++k) dst[m][k] = *(const LAS bf16x8*)(lds + PG8_SA(b, h) + aoff + m * 2048 + k * 1024); } while (0)
; #define PG8_MMA(ai, bj, At, Bt) do { __builtin_amdgcn_s_setprio(1); _Pragma("unroll") for (int m = 0; m < 4; ++m) _Pragma("unroll") for (int n = 0; n < 2; ++n) _Pragma("unroll") for (int k = 0; k < 2; ++k) \
;         acc[ai][bj][m][n] = __builtin_amdgcn_mfma_f32_16x16x32_bf16(Bt[n][k], At[m][k], acc[ai][bj][m][n], 0, 0, 0); __builtin_amdgcn_s_setprio(0); } while (0)
; #define PG8_WAIT_V(n) asm volatile("s_waitcnt vmcnt(" #n ")" ::: "memory")
; #define PG8_WAIT_L(n) asm volatile("s_waitcnt lgkmcnt(" #n ")" ::: "memory")
; #define PG8_BAR __builtin_amdgcn_s_barrier()
; #define PG8_SCHED __builtin_amdgcn_sched_barrier(0)
; template <class Epi, class Sched, bool GATHER = false>
; __device__ __forceinline__ void gemm_phase(LAS unsigned char* lds, const int lda, const int ldb, const int K, const Sched& S, const Epi& E, const int* gidx = nullptr) {
;     ...
;             PG8_LDA(At, 1, 1); PG8_STAGE(PG8_SB(1, 0), b3, voffB); PG8_STAGE(PG8_SB(1, 1), b3 + hstepB, voffB); PG8_STAGE(PG8_SA(1, 0), a3, o2[0]);
;             PG8_WAIT_V(8); PG8_WAIT_L(0); PG8_BAR; PG8_MMA(1, 0, At, B0); PG8_MMA(1, 1, At, B1); PG8_BAR; PG8_SCHED;
;         }
;         if (wr == 0) PG8_BAR;
	ds_read_b128 v[182:185], v229 offset:49152
	ds_read_b128 v[186:189], v229 offset:50176
	ds_read_b128 v[190:193], v229 offset:51200
	ds_read_b128 v[196:199], v229 offset:52224
	ds_read_b128 v[200:203], v229 offset:53248
	ds_read_b128 v[204:207], v229 offset:54272
	ds_read_b128 v[208:211], v229 offset:55296
	ds_read_b128 v[230:233], v229 offset:56320
	s_add_i32 s28, s28, s43
	v_lshl_add_u64 v[234:235], v[234:235], 0, s[64:65]
	s_mov_b32 m0, s28
	s_nop 0
	global_load_lds_dwordx4 v[234:235], off
	s_add_i32 m0, s28, 0x2000
	s_add_u32 s12, s12, 0x80080
	v_lshl_add_u64 v[234:235], v[236:237], 0, s[64:65]
	s_addc_u32 s13, s13, 0
	s_add_i32 s28, s29, s43
	global_load_lds_dwordx4 v[234:235], off
	v_lshl_add_u64 v[234:235], s[12:13], 0, v[162:163]
	s_mov_b32 m0, s28
	s_nop 0
	global_load_lds_dwordx4 v[234:235], off
	v_lshl_add_u64 v[234:235], s[12:13], 0, v[164:165]
	s_add_i32 m0, s28, 0x2000
	s_nop 0
	global_load_lds_dwordx4 v[234:235], off
	v_lshl_add_u64 v[234:235], v[238:239], 0, s[64:65]
	s_mov_b32 m0, s10
	s_nop 0
	global_load_lds_dwordx4 v[234:235], off
	v_lshl_add_u64 v[234:235], v[240:241], 0, s[64:65]
	s_mov_b32 m0, s11
	s_nop 0
	global_load_lds_dwordx4 v[234:235], off
	s_waitcnt vmcnt(8)
	s_waitcnt lgkmcnt(0)
	s_barrier
	v_mfma_f32_16x16x32_bf16 v[62:65], v[126:129], v[182:185], v[62:65]
	v_mfma_f32_16x16x32_bf16 v[58:61], v[138:141], v[182:185], v[58:61]
	v_mfma_f32_16x16x32_bf16 v[46:49], v[126:129], v[190:193], v[46:49]
	v_mfma_f32_16x16x32_bf16 v[42:45], v[138:141], v[190:193], v[42:45]
	v_mfma_f32_16x16x32_bf16 v[30:33], v[126:129], v[200:203], v[30:33]
	v_mfma_f32_16x16x32_bf16 v[26:29], v[138:141], v[200:203], v[26:29]
	v_mfma_f32_16x16x32_bf16 v[14:17], v[126:129], v[208:211], v[14:17]
	v_mfma_f32_16x16x32_bf16 v[10:13], v[138:141], v[208:211], v[10:13]
	v_mfma_f32_16x16x32_bf16 v[62:65], v[130:133], v[186:189], v[62:65]
	v_mfma_f32_16x16x32_bf16 v[58:61], v[142:145], v[186:189], v[58:61]
	v_mfma_f32_16x16x32_bf16 v[46:49], v[130:133], v[196:199], v[46:49]
	v_mfma_f32_16x16x32_bf16 v[42:45], v[142:145], v[196:199], v[42:45]
	v_mfma_f32_16x16x32_bf16 v[30:33], v[130:133], v[204:207], v[30:33]
	v_mfma_f32_16x16x32_bf16 v[26:29], v[142:145], v[204:207], v[26:29]
	v_mfma_f32_16x16x32_bf16 v[14:17], v[130:133], v[230:233], v[14:17]
	v_mfma_f32_16x16x32_bf16 v[10:13], v[142:145], v[230:233], v[10:13]
	v_mfma_f32_16x16x32_bf16 v[54:57], v[146:149], v[182:185], v[54:57]
	v_mfma_f32_16x16x32_bf16 v[50:53], v[154:157], v[182:185], v[50:53]
	v_mfma_f32_16x16x32_bf16 v[38:41], v[146:149], v[190:193], v[38:41]
	v_mfma_f32_16x16x32_bf16 v[34:37], v[154:157], v[190:193], v[34:37]
	v_mfma_f32_16x16x32_bf16 v[22:25], v[146:149], v[200:203], v[22:25]
	v_mfma_f32_16x16x32_bf16 v[18:21], v[154:157], v[200:203], v[18:21]
	v_mfma_f32_16x16x32_bf16 v[6:9], v[146:149], v[208:211], v[6:9]
	v_mfma_f32_16x16x32_bf16 v[2:5], v[154:157], v[208:211], v[2:5]
	v_mfma_f32_16x16x32_bf16 v[54:57], v[150:153], v[186:189], v[54:57]
	v_mfma_f32_16x16x32_bf16 v[50:53], v[158:161], v[186:189], v[50:53]
	v_mfma_f32_16x16x32_bf16 v[38:41], v[150:153], v[196:199], v[38:41]
	v_mfma_f32_16x16x32_bf16 v[34:37], v[158:161], v[196:199], v[34:37]
	v_mfma_f32_16x16x32_bf16 v[22:25], v[150:153], v[204:207], v[22:25]
	v_mfma_f32_16x16x32_bf16 v[18:21], v[158:161], v[204:207], v[18:21]
	v_mfma_f32_16x16x32_bf16 v[6:9], v[150:153], v[230:233], v[6:9]
	v_mfma_f32_16x16x32_bf16 v[2:5], v[158:161], v[230:233], v[2:5]
	s_barrier
	s_add_i32 s75, s75, 2
	s_add_u32 s72, s72, 0x100
	s_addc_u32 s73, s73, 0
	s_add_u32 s60, s60, 0x100
	s_addc_u32 s74, s74, 0
	s_cmp_gt_u32 s75, 29
	s_cbranch_scc0 .LBB0_428
	s_and_b64 vcc, exec, s[48:49]
	s_cbranch_vccz .LBB0_431
	s_barrier

; #define PG8_AOFF(of, u) do { _Pragma("unroll") for (int hh_ = 0; hh_ < 2; ++hh_) _Pragma("unroll") for (int i_ = 0; i_ < 2; ++i_) { \
;         if constexpr (GATHER) of[hh_][i_] = (unsigned)gidx[(u).pm * 256 + hh_ * 128 + RA[i_]] * (unsigned)(lda * 2) + CA2[i_]; \
;         else of[hh_][i_] = (unsigned)((hh_ * HALF + RA[i_]) * lda) * 2u + CA2[i_]; } } while (0)
; #define PG8_STAGE(bufoff, gbase, voff) do { _Pragma("unroll") for (int _i = 0; _i < 2; ++_i) \
;         __builtin_amdgcn_global_load_lds((const unsigned*)((const char*)(gbase) + (voff)[_i]), (LAS unsigned*)(lds + (bufoff) + ldsw + _i * 8192), 16, 0, 0); } while (0)
; #define PG8_LDA(dst, b, h) do { _Pragma("unroll") for (int m = 0; m < 4; ++m) _Pragma("unroll") for (int k = 0; k < 2; ++k) dst[m][k] = *(const LAS bf16x8*)(lds + PG8_SA(b, h) + aoff + m * 2048 + k * 1024); } while (0)
; #define PG8_WAIT_V(n) asm volatile("s_waitcnt vmcnt(" #n ")" ::: "memory")
; #define PG8_WAIT_L(n) asm volatile("s_waitcnt lgkmcnt(" #n ")" ::: "memory")
; template <class Epi, class Sched, bool GATHER = false>
; __device__ __forceinline__ void gemm_phase(LAS unsigned char* lds, const int lda, const int ldb, const int K, const Sched& S, const Epi& E, const int* gidx = nullptr) {
;     ...
;             const bool last = (t == nt - 2);
;             if constexpr (GATHER) { if (last && has_next) PG8_AOFF(ofn, nxt); }
;             const char* a1 = cA + (size_t)(t + 1) * kstep;
;             const char* a2 = last ? nA : cA + (size_t)(t + 2) * kstep; const char* b2 = last ? nB : cB + (size_t)(t + 2) * kstep;
;             const char* a3 = a2 + kstep; const char* b3 = b2 + kstep;
;             unsigned o2[2][2];
; #pragma unroll
;             for (int hh = 0; hh < 2; ++hh)
; #pragma unroll
;                 for (int i = 0; i < 2; ++i) { if constexpr (GATHER) o2[hh][i] = last ? ofn[hh][i] : ofc[hh][i]; else o2[hh][i] = ofc[hh][i]; }
;             PG8_LDB(B0, 0, 0); PG8_LDB(B1, 0, 1); PG8_SCHED; PG8_LDA(At, 0, 0); PG8_STAGE(PG8_SA(1, 1), a1, ofc[1]);
;             PG8_WAIT_V(8); PG8_WAIT_L(0); PG8_BAR; PG8_MMA(0, 0, At, B0); PG8_MMA(0, 1, At, B1); PG8_BAR; PG8_SCHED;
;             PG8_LDA(At, 0, 1); PG8_STAGE(PG8_SB(0, 0), b2, voffB); PG8_STAGE(PG8_SB(0, 1), b2 + hstepB, voffB); PG8_STAGE(PG8_SA(0, 0), a2, o2[0]);
;             PG8_WAIT_V(8); PG8_WAIT_L(0); PG8_BAR; PG8_MMA(1, 0, At, B0); PG8_MMA(1, 1, At, B1); PG8_BAR; PG8_SCHED;
.LBB0_1107:
	s_add_i32 s28, 0, 0x10000
	s_add_i32 s33, 0, 0x14000
	v_add_u32_e32 v86, s28, v178
	v_add_u32_e32 v172, s33, v178
	ds_read_b128 v[70:73], v86
	ds_read_b128 v[78:81], v86 offset:1024
	ds_read_b128 v[82:85], v86 offset:2048
	ds_read_b128 v[86:89], v86 offset:3072
	ds_read_b128 v[146:149], v172
	ds_read_b128 v[150:153], v172 offset:1024
	ds_read_b128 v[168:171], v172 offset:2048
	ds_read_b128 v[172:175], v172 offset:3072
	ds_read_b128 v[182:185], v180
	ds_read_b128 v[186:189], v180 offset:1024
	ds_read_b128 v[190:193], v180 offset:2048
	ds_read_b128 v[196:199], v180 offset:3072
	ds_read_b128 v[200:203], v180 offset:4096
	ds_read_b128 v[204:207], v180 offset:5120
	ds_read_b128 v[208:211], v180 offset:6144
	ds_read_b128 v[228:231], v180 offset:7168
	v_lshl_add_u64 v[176:177], s[34:35], 0, v[166:167]
	s_add_i32 m0, s59, 0xc000
	s_add_u32 s12, s34, 0x80
	s_addc_u32 s13, s35, 0
	s_cmp_eq_u32 s83, 28
	s_cselect_b32 s67, s71, s13
	s_cselect_b32 s66, s70, s12
	s_cselect_b32 s13, s73, s82
	s_cselect_b32 s12, s72, s69
	global_load_lds_dwordx4 v[176:177], off
	v_lshl_add_u64 v[176:177], s[34:35], 0, v[164:165]
	s_add_i32 m0, s59, 0xe000
	s_nop 0
	global_load_lds_dwordx4 v[176:177], off
	s_waitcnt vmcnt(8)
	s_waitcnt lgkmcnt(0)
	s_barrier
	v_mfma_f32_16x16x32_bf16 v[142:145], v[70:73], v[182:185], v[142:145]
	v_mfma_f32_16x16x32_bf16 v[138:141], v[82:85], v[182:185], v[138:141]
	v_mfma_f32_16x16x32_bf16 v[126:129], v[70:73], v[190:193], v[126:129]
	v_mfma_f32_16x16x32_bf16 v[122:125], v[82:85], v[190:193], v[122:125]
	v_mfma_f32_16x16x32_bf16 v[110:113], v[70:73], v[200:203], v[110:113]
	v_mfma_f32_16x16x32_bf16 v[106:109], v[82:85], v[200:203], v[106:109]
	v_mfma_f32_16x16x32_bf16 v[94:97], v[70:73], v[208:211], v[94:97]
	v_mfma_f32_16x16x32_bf16 v[90:93], v[82:85], v[208:211], v[90:93]
	v_mfma_f32_16x16x32_bf16 v[142:145], v[78:81], v[186:189], v[142:145]
	v_mfma_f32_16x16x32_bf16 v[138:141], v[86:89], v[186:189], v[138:141]
	v_mfma_f32_16x16x32_bf16 v[126:129], v[78:81], v[196:199], v[126:129]
	v_mfma_f32_16x16x32_bf16 v[122:125], v[86:89], v[196:199], v[122:125]
	v_mfma_f32_16x16x32_bf16 v[110:113], v[78:81], v[204:207], v[110:113]
	v_mfma_f32_16x16x32_bf16 v[106:109], v[86:89], v[204:207], v[106:109]
	v_mfma_f32_16x16x32_bf16 v[94:97], v[78:81], v[228:231], v[94:97]
	v_mfma_f32_16x16x32_bf16 v[90:93], v[86:89], v[228:231], v[90:93]
	v_mfma_f32_16x16x32_bf16 v[134:137], v[146:149], v[182:185], v[134:137]
	v_mfma_f32_16x16x32_bf16 v[130:133], v[168:171], v[182:185], v[130:133]
	v_mfma_f32_16x16x32_bf16 v[118:121], v[146:149], v[190:193], v[118:121]
	v_mfma_f32_16x16x32_bf16 v[114:117], v[168:171], v[190:193], v[114:117]
	v_mfma_f32_16x16x32_bf16 v[102:105], v[146:149], v[200:203], v[102:105]
	v_mfma_f32_16x16x32_bf16 v[98:101], v[168:171], v[200:203], v[98:101]
	v_mfma_f32_16x16x32_bf16 v[74:77], v[146:149], v[208:211], v[74:77]
	v_mfma_f32_16x16x32_bf16 v[66:69], v[168:171], v[208:211], v[66:69]
	v_mfma_f32_16x16x32_bf16 v[134:137], v[150:153], v[186:189], v[134:137]
	v_mfma_f32_16x16x32_bf16 v[130:133], v[172:175], v[186:189], v[130:133]
	v_mfma_f32_16x16x32_bf16 v[118:121], v[150:153], v[196:199], v[118:121]
	v_mfma_f32_16x16x32_bf16 v[114:117], v[172:175], v[196:199], v[114:117]
	v_mfma_f32_16x16x32_bf16 v[102:105], v[150:153], v[204:207], v[102:105]
	v_mfma_f32_16x16x32_bf16 v[98:101], v[172:175], v[204:207], v[98:101]
	v_mfma_f32_16x16x32_bf16 v[74:77], v[150:153], v[228:231], v[74:77]
	v_mfma_f32_16x16x32_bf16 v[66:69], v[172:175], v[228:231], v[66:69]
	s_barrier
	ds_read_b128 v[182:185], v180 offset:16384
	ds_read_b128 v[186:189], v180 offset:17408
	ds_read_b128 v[190:193], v180 offset:18432
	ds_read_b128 v[196:199], v180 offset:19456
	ds_read_b128 v[200:203], v180 offset:20480
	ds_read_b128 v[204:207], v180 offset:21504
	ds_read_b128 v[208:211], v180 offset:22528
	ds_read_b128 v[228:231], v180 offset:23552
	s_add_i32 s28, s28, s8
	v_lshl_add_u64 v[176:177], s[12:13], 0, v[194:195]
	s_mov_b32 m0, s28
	s_nop 0
	global_load_lds_dwordx4 v[176:177], off
	s_add_i32 m0, s28, 0x2000
	s_add_u32 s28, s12, 0x80000
	v_lshl_add_u64 v[232:233], s[12:13], 0, v[154:155]
	s_addc_u32 s29, s13, 0
	s_add_i32 s33, s33, s8
	global_load_lds_dwordx4 v[232:233], off
	v_lshl_add_u64 v[234:235], s[28:29], 0, v[194:195]
	s_mov_b32 m0, s33
	v_lshl_add_u64 v[236:237], s[66:67], 0, v[158:159]
	global_load_lds_dwordx4 v[234:235], off
	v_lshl_add_u64 v[234:235], s[28:29], 0, v[154:155]
	s_add_i32 m0, s33, 0x2000
	s_nop 0
	global_load_lds_dwordx4 v[234:235], off
	v_lshl_add_u64 v[234:235], s[66:67], 0, v[156:157]
	s_mov_b32 m0, s59
	s_nop 0
	global_load_lds_dwordx4 v[234:235], off
	s_mov_b32 m0, s60
	s_nop 0
	global_load_lds_dwordx4 v[236:237], off
	s_waitcnt vmcnt(8)
	s_waitcnt lgkmcnt(0)
	s_barrier
; #define PG8_STAGE(bufoff, gbase, voff) do { _Pragma("unroll") for (int _i = 0; _i < 2; ++_i) \
;         __builtin_amdgcn_global_load_lds((const unsigned*)((const char*)(gbase) + (voff)[_i]), (LAS unsigned*)(lds + (bufoff) + ldsw + _i * 8192), 16, 0, 0); } while (0)
; #define PG8_LDA(dst, b, h) do { _Pragma("unroll") for (int m = 0; m < 4; ++m) _Pragma("unroll") for (int k = 0; k < 2; ++k) dst[m][k] = *(const LAS bf16x8*)(lds + PG8_SA(b, h) + aoff + m * 2048 + k * 1024); } while (0)
; #define PG8_LDB(dst, b, h) do { _Pragma("unroll") for (int n = 0; n < 2; ++n) _Pragma("unroll") for (int k = 0; k < 2; ++k) dst[n][k] = *(const LAS bf16x8*)(lds + PG8_SB(b, h) + boff + n * 2048 + k * 1024); } while (0)
; #define PG8_MMA(ai, bj, At, Bt) do { __builtin_amdgcn_s_setprio(1); _Pragma("unroll") for (int m = 0; m < 4; ++m) _Pragma("unroll") for (int n = 0; n < 2; ++n) _Pragma("unroll") for (int k = 0; k < 2; ++k) \
;         acc[ai][bj][m][n] = __builtin_amdgcn_mfma_f32_16x16x32_bf16(Bt[n][k], At[m][k], acc[ai][bj][m][n], 0, 0, 0); __builtin_amdgcn_s_setprio(0); } while (0)
; #define PG8_WAIT_V(n) asm volatile("s_waitcnt vmcnt(" #n ")" ::: "memory")
; #define PG8_WAIT_L(n) asm volatile("s_waitcnt lgkmcnt(" #n ")" ::: "memory")
; #define PG8_BAR __builtin_amdgcn_s_barrier()
; #define PG8_SCHED __builtin_amdgcn_sched_barrier(0)
; template <class Epi, class Sched, bool GATHER = false>
; __device__ __forceinline__ void gemm_phase(LAS unsigned char* lds, const int lda, const int ldb, const int K, const Sched& S, const Epi& E, const int* gidx = nullptr) {
;     ...
;             PG8_WAIT_V(8); PG8_WAIT_L(0); PG8_BAR; PG8_MMA(1, 0, At, B0); PG8_MMA(1, 1, At, B1); PG8_BAR; PG8_SCHED;
;             PG8_LDB(B0, 1, 0); PG8_LDB(B1, 1, 1); PG8_SCHED; PG8_LDA(At, 1, 0); PG8_STAGE(PG8_SA(0, 1), a2, o2[1]);
;             PG8_WAIT_V(8); PG8_WAIT_L(0); PG8_BAR; PG8_MMA(0, 0, At, B0); PG8_MMA(0, 1, At, B1); PG8_BAR; PG8_SCHED;
	v_mfma_f32_16x16x32_bf16 v[62:65], v[70:73], v[182:185], v[62:65]
	v_mfma_f32_16x16x32_bf16 v[58:61], v[82:85], v[182:185], v[58:61]
	v_mfma_f32_16x16x32_bf16 v[46:49], v[70:73], v[190:193], v[46:49]
	v_mfma_f32_16x16x32_bf16 v[38:41], v[82:85], v[190:193], v[38:41]
	v_mfma_f32_16x16x32_bf16 v[26:29], v[70:73], v[200:203], v[26:29]
	v_mfma_f32_16x16x32_bf16 v[18:21], v[82:85], v[200:203], v[18:21]
	v_mfma_f32_16x16x32_bf16 v[6:9], v[70:73], v[208:211], v[6:9]
	v_mfma_f32_16x16x32_bf16 v[2:5], v[82:85], v[208:211], v[2:5]
	v_mfma_f32_16x16x32_bf16 v[62:65], v[78:81], v[186:189], v[62:65]
	v_mfma_f32_16x16x32_bf16 v[58:61], v[86:89], v[186:189], v[58:61]
	v_mfma_f32_16x16x32_bf16 v[46:49], v[78:81], v[196:199], v[46:49]
	v_mfma_f32_16x16x32_bf16 v[38:41], v[86:89], v[196:199], v[38:41]
	v_mfma_f32_16x16x32_bf16 v[26:29], v[78:81], v[204:207], v[26:29]
	v_mfma_f32_16x16x32_bf16 v[18:21], v[86:89], v[204:207], v[18:21]
	v_mfma_f32_16x16x32_bf16 v[6:9], v[78:81], v[228:231], v[6:9]
	v_mfma_f32_16x16x32_bf16 v[2:5], v[86:89], v[228:231], v[2:5]
	v_mfma_f32_16x16x32_bf16 v[54:57], v[146:149], v[182:185], v[54:57]
	v_mfma_f32_16x16x32_bf16 v[50:53], v[168:171], v[182:185], v[50:53]
	v_mfma_f32_16x16x32_bf16 v[42:45], v[146:149], v[190:193], v[42:45]
	v_mfma_f32_16x16x32_bf16 v[34:37], v[168:171], v[190:193], v[34:37]
	v_mfma_f32_16x16x32_bf16 v[30:33], v[146:149], v[200:203], v[30:33]
	v_mfma_f32_16x16x32_bf16 v[22:25], v[168:171], v[200:203], v[22:25]
	v_mfma_f32_16x16x32_bf16 v[14:17], v[146:149], v[208:211], v[14:17]
	v_mfma_f32_16x16x32_bf16 v[10:13], v[168:171], v[208:211], v[10:13]
	v_mfma_f32_16x16x32_bf16 v[54:57], v[150:153], v[186:189], v[54:57]
	v_mfma_f32_16x16x32_bf16 v[50:53], v[172:175], v[186:189], v[50:53]
	v_mfma_f32_16x16x32_bf16 v[42:45], v[150:153], v[196:199], v[42:45]
	v_mfma_f32_16x16x32_bf16 v[34:37], v[172:175], v[196:199], v[34:37]
	v_mfma_f32_16x16x32_bf16 v[30:33], v[150:153], v[204:207], v[30:33]
	v_mfma_f32_16x16x32_bf16 v[22:25], v[172:175], v[204:207], v[22:25]
	v_mfma_f32_16x16x32_bf16 v[14:17], v[150:153], v[228:231], v[14:17]
	v_mfma_f32_16x16x32_bf16 v[10:13], v[172:175], v[228:231], v[10:13]
	s_barrier
	s_add_i32 s28, 0, 0x18000
	s_add_i32 s29, 0, 0x1c000
	v_add_u32_e32 v86, s28, v178
	v_add_u32_e32 v172, s29, v178
	ds_read_b128 v[70:73], v86
	ds_read_b128 v[78:81], v86 offset:1024
	ds_read_b128 v[82:85], v86 offset:2048
	ds_read_b128 v[86:89], v86 offset:3072
	ds_read_b128 v[146:149], v172
	ds_read_b128 v[150:153], v172 offset:1024
	ds_read_b128 v[168:171], v172 offset:2048
	ds_read_b128 v[172:175], v172 offset:3072
	ds_read_b128 v[182:185], v180 offset:32768
	ds_read_b128 v[186:189], v180 offset:33792
	ds_read_b128 v[190:193], v180 offset:34816
	ds_read_b128 v[196:199], v180 offset:35840
	ds_read_b128 v[200:203], v180 offset:36864
	ds_read_b128 v[204:207], v180 offset:37888
	ds_read_b128 v[208:211], v180 offset:38912
	ds_read_b128 v[228:231], v180 offset:39936
	s_mov_b32 m0, s74
	v_lshl_add_u64 v[238:239], s[66:67], 0, v[160:161]
	global_load_lds_dwordx4 v[238:239], off
	v_lshl_add_u64 v[238:239], s[66:67], 0, v[162:163]
	s_mov_b32 m0, s75
	s_nop 0
	global_load_lds_dwordx4 v[238:239], off
	s_waitcnt vmcnt(8)
	s_waitcnt lgkmcnt(0)
	s_barrier
	v_mfma_f32_16x16x32_bf16 v[142:145], v[70:73], v[182:185], v[142:145]
	v_mfma_f32_16x16x32_bf16 v[138:141], v[82:85], v[182:185], v[138:141]
	v_mfma_f32_16x16x32_bf16 v[126:129], v[70:73], v[190:193], v[126:129]
	v_mfma_f32_16x16x32_bf16 v[122:125], v[82:85], v[190:193], v[122:125]
	v_mfma_f32_16x16x32_bf16 v[110:113], v[70:73], v[200:203], v[110:113]
	v_mfma_f32_16x16x32_bf16 v[106:109], v[82:85], v[200:203], v[106:109]
	v_mfma_f32_16x16x32_bf16 v[94:97], v[70:73], v[208:211], v[94:97]
	v_mfma_f32_16x16x32_bf16 v[90:93], v[82:85], v[208:211], v[90:93]
	v_mfma_f32_16x16x32_bf16 v[142:145], v[78:81], v[186:189], v[142:145]
	v_mfma_f32_16x16x32_bf16 v[138:141], v[86:89], v[186:189], v[138:141]
	v_mfma_f32_16x16x32_bf16 v[126:129], v[78:81], v[196:199], v[126:129]
	v_mfma_f32_16x16x32_bf16 v[122:125], v[86:89], v[196:199], v[122:125]
	v_mfma_f32_16x16x32_bf16 v[110:113], v[78:81], v[204:207], v[110:113]
	v_mfma_f32_16x16x32_bf16 v[106:109], v[86:89], v[204:207], v[106:109]
	v_mfma_f32_16x16x32_bf16 v[94:97], v[78:81], v[228:231], v[94:97]
	v_mfma_f32_16x16x32_bf16 v[90:93], v[86:89], v[228:231], v[90:93]
	v_mfma_f32_16x16x32_bf16 v[134:137], v[146:149], v[182:185], v[134:137]
	v_mfma_f32_16x16x32_bf16 v[130:133], v[168:171], v[182:185], v[130:133]
	v_mfma_f32_16x16x32_bf16 v[118:121], v[146:149], v[190:193], v[118:121]
	v_mfma_f32_16x16x32_bf16 v[114:117], v[168:171], v[190:193], v[114:117]
	v_mfma_f32_16x16x32_bf16 v[102:105], v[146:149], v[200:203], v[102:105]
	v_mfma_f32_16x16x32_bf16 v[98:101], v[168:171], v[200:203], v[98:101]
	v_mfma_f32_16x16x32_bf16 v[74:77], v[146:149], v[208:211], v[74:77]
	v_mfma_f32_16x16x32_bf16 v[66:69], v[168:171], v[208:211], v[66:69]
	v_mfma_f32_16x16x32_bf16 v[134:137], v[150:153], v[186:189], v[134:137]
	v_mfma_f32_16x16x32_bf16 v[130:133], v[172:175], v[186:189], v[130:133]
	v_mfma_f32_16x16x32_bf16 v[118:121], v[150:153], v[196:199], v[118:121]
	v_mfma_f32_16x16x32_bf16 v[114:117], v[172:175], v[196:199], v[114:117]
	v_mfma_f32_16x16x32_bf16 v[102:105], v[150:153], v[204:207], v[102:105]
	v_mfma_f32_16x16x32_bf16 v[98:101], v[172:175], v[204:207], v[98:101]
	v_mfma_f32_16x16x32_bf16 v[74:77], v[150:153], v[228:231], v[74:77]
	v_mfma_f32_16x16x32_bf16 v[66:69], v[172:175], v[228:231], v[66:69]
	s_barrier
; #define PG8_STAGE(bufoff, gbase, voff) do { _Pragma("unroll") for (int _i = 0; _i < 2; ++_i) \
;         __builtin_amdgcn_global_load_lds((const unsigned*)((const char*)(gbase) + (voff)[_i]), (LAS unsigned*)(lds + (bufoff) + ldsw + _i * 8192), 16, 0, 0); } while (0)
; #define PG8_LDA(dst, b, h) do { _Pragma("unroll") for (int m = 0; m < 4; ++m) _Pragma("unroll") for (int k = 0; k < 2; ++k) dst[m][k] = *(const LAS bf16x8*)(lds + PG8_SA(b, h) + aoff + m * 2048 + k * 1024); } while (0)
; #define PG8_MMA(ai, bj, At, Bt) do { __builtin_amdgcn_s_setprio(1); _Pragma("unroll") for (int m = 0; m < 4; ++m) _Pragma("unroll") for (int n = 0; n < 2; ++n) _Pragma("unroll") for (int k = 0; k < 2; ++k) \
;         acc[ai][bj][m][n] = __builtin_amdgcn_mfma_f32_16x16x32_bf16(Bt[n][k], At[m][k], acc[ai][bj][m][n], 0, 0, 0); __builtin_amdgcn_s_setprio(0); } while (0)
; #define PG8_WAIT_V(n) asm volatile("s_waitcnt vmcnt(" #n ")" ::: "memory")
; #define PG8_WAIT_L(n) asm volatile("s_waitcnt lgkmcnt(" #n ")" ::: "memory")
; #define PG8_BAR __builtin_amdgcn_s_barrier()
; #define PG8_SCHED __builtin_amdgcn_sched_barrier(0)
; template <class Epi, class Sched, bool GATHER = false>
; __device__ __forceinline__ void gemm_phase(LAS unsigned char* lds, const int lda, const int ldb, const int K, const Sched& S, const Epi& E, const int* gidx = nullptr) {
;     ...
;             PG8_LDA(At, 1, 1); PG8_STAGE(PG8_SB(1, 0), b3, voffB); PG8_STAGE(PG8_SB(1, 1), b3 + hstepB, voffB); PG8_STAGE(PG8_SA(1, 0), a3, o2[0]);
;             PG8_WAIT_V(8); PG8_WAIT_L(0); PG8_BAR; PG8_MMA(1, 0, At, B0); PG8_MMA(1, 1, At, B1); PG8_BAR; PG8_SCHED;
;         }
;         if (wr == 0) PG8_BAR;
	ds_read_b128 v[182:185], v180 offset:49152
	ds_read_b128 v[186:189], v180 offset:50176
	ds_read_b128 v[190:193], v180 offset:51200
	ds_read_b128 v[196:199], v180 offset:52224
	ds_read_b128 v[200:203], v180 offset:53248
	ds_read_b128 v[204:207], v180 offset:54272
	ds_read_b128 v[208:211], v180 offset:55296
	ds_read_b128 v[228:231], v180 offset:56320
	s_add_i32 s28, s28, s8
	v_lshl_add_u64 v[176:177], v[176:177], 0, s[64:65]
	s_mov_b32 m0, s28
	s_nop 0
	global_load_lds_dwordx4 v[176:177], off
	s_add_i32 m0, s28, 0x2000
	s_add_u32 s12, s12, 0x80080
	v_lshl_add_u64 v[176:177], v[232:233], 0, s[64:65]
	s_addc_u32 s13, s13, 0
	s_add_i32 s28, s29, s8
	global_load_lds_dwordx4 v[176:177], off
	v_lshl_add_u64 v[176:177], s[12:13], 0, v[194:195]
	s_mov_b32 m0, s28
	s_nop 0
	global_load_lds_dwordx4 v[176:177], off
	v_lshl_add_u64 v[176:177], s[12:13], 0, v[154:155]
	s_add_i32 m0, s28, 0x2000
	s_nop 0
	global_load_lds_dwordx4 v[176:177], off
	v_lshl_add_u64 v[176:177], v[234:235], 0, s[64:65]
	s_mov_b32 m0, s76
	s_nop 0
	global_load_lds_dwordx4 v[176:177], off
	v_lshl_add_u64 v[176:177], v[236:237], 0, s[64:65]
	s_mov_b32 m0, s77
	s_nop 0
	global_load_lds_dwordx4 v[176:177], off
	s_waitcnt vmcnt(8)
	s_waitcnt lgkmcnt(0)
	s_barrier
	v_mfma_f32_16x16x32_bf16 v[62:65], v[70:73], v[182:185], v[62:65]
	v_mfma_f32_16x16x32_bf16 v[58:61], v[82:85], v[182:185], v[58:61]
	v_mfma_f32_16x16x32_bf16 v[46:49], v[70:73], v[190:193], v[46:49]
	v_mfma_f32_16x16x32_bf16 v[38:41], v[82:85], v[190:193], v[38:41]
	v_mfma_f32_16x16x32_bf16 v[26:29], v[70:73], v[200:203], v[26:29]
	v_mfma_f32_16x16x32_bf16 v[18:21], v[82:85], v[200:203], v[18:21]
	v_mfma_f32_16x16x32_bf16 v[6:9], v[70:73], v[208:211], v[6:9]
	v_mfma_f32_16x16x32_bf16 v[2:5], v[82:85], v[208:211], v[2:5]
	v_mfma_f32_16x16x32_bf16 v[62:65], v[78:81], v[186:189], v[62:65]
	v_mfma_f32_16x16x32_bf16 v[58:61], v[86:89], v[186:189], v[58:61]
	v_mfma_f32_16x16x32_bf16 v[46:49], v[78:81], v[196:199], v[46:49]
	v_mfma_f32_16x16x32_bf16 v[38:41], v[86:89], v[196:199], v[38:41]
	v_mfma_f32_16x16x32_bf16 v[26:29], v[78:81], v[204:207], v[26:29]
	v_mfma_f32_16x16x32_bf16 v[18:21], v[86:89], v[204:207], v[18:21]
	v_mfma_f32_16x16x32_bf16 v[6:9], v[78:81], v[228:231], v[6:9]
	v_mfma_f32_16x16x32_bf16 v[2:5], v[86:89], v[228:231], v[2:5]
	v_mfma_f32_16x16x32_bf16 v[54:57], v[146:149], v[182:185], v[54:57]
	v_mfma_f32_16x16x32_bf16 v[50:53], v[168:171], v[182:185], v[50:53]
	v_mfma_f32_16x16x32_bf16 v[42:45], v[146:149], v[190:193], v[42:45]
	v_mfma_f32_16x16x32_bf16 v[34:37], v[168:171], v[190:193], v[34:37]
	v_mfma_f32_16x16x32_bf16 v[30:33], v[146:149], v[200:203], v[30:33]
	v_mfma_f32_16x16x32_bf16 v[22:25], v[168:171], v[200:203], v[22:25]
	v_mfma_f32_16x16x32_bf16 v[14:17], v[146:149], v[208:211], v[14:17]
	v_mfma_f32_16x16x32_bf16 v[10:13], v[168:171], v[208:211], v[10:13]
	v_mfma_f32_16x16x32_bf16 v[54:57], v[150:153], v[186:189], v[54:57]
	v_mfma_f32_16x16x32_bf16 v[50:53], v[172:175], v[186:189], v[50:53]
	v_mfma_f32_16x16x32_bf16 v[42:45], v[150:153], v[196:199], v[42:45]
	v_mfma_f32_16x16x32_bf16 v[34:37], v[172:175], v[196:199], v[34:37]
	v_mfma_f32_16x16x32_bf16 v[30:33], v[150:153], v[204:207], v[30:33]
	v_mfma_f32_16x16x32_bf16 v[22:25], v[172:175], v[204:207], v[22:25]
	v_mfma_f32_16x16x32_bf16 v[14:17], v[150:153], v[228:231], v[14:17]
	v_mfma_f32_16x16x32_bf16 v[10:13], v[172:175], v[228:231], v[10:13]
	s_barrier
	s_add_i32 s83, s83, 2
	s_add_u32 s34, s34, 0x100
	s_addc_u32 s35, s35, 0
	s_add_u32 s69, s69, 0x100
	s_addc_u32 s82, s82, 0
	s_cmp_gt_u32 s83, 29
	s_cbranch_scc0 .LBB0_1107
	s_and_b64 vcc, exec, s[48:49]
	s_cbranch_vccz .LBB0_1110
	s_barrier

; #define PG8_AOFF(of, u) do { _Pragma("unroll") for (int hh_ = 0; hh_ < 2; ++hh_) _Pragma("unroll") for (int i_ = 0; i_ < 2; ++i_) { \
;         if constexpr (GATHER) of[hh_][i_] = (unsigned)gidx[(u).pm * 256 + hh_ * 128 + RA[i_]] * (unsigned)(lda * 2) + CA2[i_]; \
;         else of[hh_][i_] = (unsigned)((hh_ * HALF + RA[i_]) * lda) * 2u + CA2[i_]; } } while (0)
; #define PG8_STAGE(bufoff, gbase, voff) do { _Pragma("unroll") for (int _i = 0; _i < 2; ++_i) \
;         __builtin_amdgcn_global_load_lds((const unsigned*)((const char*)(gbase) + (voff)[_i]), (LAS unsigned*)(lds + (bufoff) + ldsw + _i * 8192), 16, 0, 0); } while (0)
; #define PG8_LDA(dst, b, h) do { _Pragma("unroll") for (int m = 0; m < 4; ++m) _Pragma("unroll") for (int k = 0; k < 2; ++k) dst[m][k] = *(const LAS bf16x8*)(lds + PG8_SA(b, h) + aoff + m * 2048 + k * 1024); } while (0)
; #define PG8_WAIT_V(n) asm volatile("s_waitcnt vmcnt(" #n ")" ::: "memory")
; #define PG8_WAIT_L(n) asm volatile("s_waitcnt lgkmcnt(" #n ")" ::: "memory")
; template <class Epi, class Sched, bool GATHER = false>
; __device__ __forceinline__ void gemm_phase(LAS unsigned char* lds, const int lda, const int ldb, const int K, const Sched& S, const Epi& E, const int* gidx = nullptr) {
;     ...
;             const bool last = (t == nt - 2);
;             if constexpr (GATHER) { if (last && has_next) PG8_AOFF(ofn, nxt); }
;             const char* a1 = cA + (size_t)(t + 1) * kstep;
;             const char* a2 = last ? nA : cA + (size_t)(t + 2) * kstep; const char* b2 = last ? nB : cB + (size_t)(t + 2) * kstep;
;             const char* a3 = a2 + kstep; const char* b3 = b2 + kstep;
;             unsigned o2[2][2];
; #pragma unroll
;             for (int hh = 0; hh < 2; ++hh)
; #pragma unroll
;                 for (int i = 0; i < 2; ++i) { if constexpr (GATHER) o2[hh][i] = last ? ofn[hh][i] : ofc[hh][i]; else o2[hh][i] = ofc[hh][i]; }
;             PG8_LDB(B0, 0, 0); PG8_LDB(B1, 0, 1); PG8_SCHED; PG8_LDA(At, 0, 0); PG8_STAGE(PG8_SA(1, 1), a1, ofc[1]);
;             PG8_WAIT_V(8); PG8_WAIT_L(0); PG8_BAR; PG8_MMA(0, 0, At, B0); PG8_MMA(0, 1, At, B1); PG8_BAR; PG8_SCHED;
;             PG8_LDA(At, 0, 1); PG8_STAGE(PG8_SB(0, 0), b2, voffB); PG8_STAGE(PG8_SB(0, 1), b2 + hstepB, voffB); PG8_STAGE(PG8_SA(0, 0), a2, o2[0]);
;             PG8_WAIT_V(8); PG8_WAIT_L(0); PG8_BAR; PG8_MMA(1, 0, At, B0); PG8_MMA(1, 1, At, B1); PG8_BAR; PG8_SCHED;
.LBB0_1186:
	s_add_i32 s28, 0, 0x10000
	s_add_i32 s33, 0, 0x14000
	v_add_u32_e32 v102, s28, v84
	v_add_u32_e32 v118, s33, v84
	ds_read_b128 v[90:93], v102
	ds_read_b128 v[94:97], v102 offset:1024
	ds_read_b128 v[98:101], v102 offset:2048
	ds_read_b128 v[102:105], v102 offset:3072
	ds_read_b128 v[106:109], v118
	ds_read_b128 v[110:113], v118 offset:1024
	ds_read_b128 v[114:117], v118 offset:2048
	ds_read_b128 v[118:121], v118 offset:3072
	ds_read_b128 v[130:133], v85
	ds_read_b128 v[134:137], v85 offset:1024
	ds_read_b128 v[186:189], v85 offset:2048
	ds_read_b128 v[190:193], v85 offset:3072
	ds_read_b128 v[196:199], v85 offset:4096
	ds_read_b128 v[200:203], v85 offset:5120
	ds_read_b128 v[208:211], v85 offset:6144
	ds_read_b128 v[228:231], v85 offset:7168
	v_lshl_add_u64 v[204:205], v[82:83], 0, s[12:13]
	s_add_i32 m0, s51, 0xc000
	s_add_u32 s28, s74, s12
	s_addc_u32 s29, s75, s13
	s_add_u32 s28, s28, 0x100
	s_addc_u32 s29, s29, 0
	s_add_u32 s33, s68, s12
	s_addc_u32 s34, s69, s13
	s_cmpk_eq_i32 s12, 0xf00
	s_cselect_b32 s49, s75, s29
	s_cselect_b32 s48, s74, s28
	s_cselect_b32 s35, s45, s34
	s_cselect_b32 s34, s44, s33
	s_add_i32 s28, 0, 0x10000
	s_add_i32 s33, 0, 0x14000
	global_load_lds_dwordx4 v[204:205], off
	v_lshl_add_u64 v[204:205], v[80:81], 0, s[12:13]
	s_add_i32 m0, s51, 0xe000
	s_nop 0
	global_load_lds_dwordx4 v[204:205], off
	s_waitcnt vmcnt(8)
	s_waitcnt lgkmcnt(0)
	s_barrier
	v_mfma_f32_16x16x32_bf16 v[182:185], v[90:93], v[130:133], v[182:185]
	v_mfma_f32_16x16x32_bf16 v[178:181], v[98:101], v[130:133], v[178:181]
	v_mfma_f32_16x16x32_bf16 v[166:169], v[90:93], v[186:189], v[166:169]
	v_mfma_f32_16x16x32_bf16 v[162:165], v[98:101], v[186:189], v[162:165]
	v_mfma_f32_16x16x32_bf16 v[150:153], v[90:93], v[196:199], v[150:153]
	v_mfma_f32_16x16x32_bf16 v[146:149], v[98:101], v[196:199], v[146:149]
	v_mfma_f32_16x16x32_bf16 v[126:129], v[90:93], v[208:211], v[126:129]
	v_mfma_f32_16x16x32_bf16 v[122:125], v[98:101], v[208:211], v[122:125]
	v_mfma_f32_16x16x32_bf16 v[182:185], v[94:97], v[134:137], v[182:185]
	v_mfma_f32_16x16x32_bf16 v[178:181], v[102:105], v[134:137], v[178:181]
	v_mfma_f32_16x16x32_bf16 v[166:169], v[94:97], v[190:193], v[166:169]
	v_mfma_f32_16x16x32_bf16 v[162:165], v[102:105], v[190:193], v[162:165]
	v_mfma_f32_16x16x32_bf16 v[150:153], v[94:97], v[200:203], v[150:153]
	v_mfma_f32_16x16x32_bf16 v[146:149], v[102:105], v[200:203], v[146:149]
	v_mfma_f32_16x16x32_bf16 v[126:129], v[94:97], v[228:231], v[126:129]
	v_mfma_f32_16x16x32_bf16 v[122:125], v[102:105], v[228:231], v[122:125]
	v_mfma_f32_16x16x32_bf16 v[174:177], v[106:109], v[130:133], v[174:177]
	v_mfma_f32_16x16x32_bf16 v[130:133], v[114:117], v[130:133], v[170:173]
	v_mfma_f32_16x16x32_bf16 v[154:157], v[114:117], v[186:189], v[154:157]
	v_mfma_f32_16x16x32_bf16 v[142:145], v[106:109], v[196:199], v[142:145]
	v_mfma_f32_16x16x32_bf16 v[138:141], v[114:117], v[196:199], v[138:141]
	v_mfma_f32_16x16x32_bf16 v[86:89], v[106:109], v[208:211], v[86:89]
	v_mfma_f32_16x16x32_bf16 v[74:77], v[114:117], v[208:211], v[74:77]
	v_mfma_f32_16x16x32_bf16 v[174:177], v[110:113], v[134:137], v[174:177]
	v_mfma_f32_16x16x32_bf16 v[130:133], v[118:121], v[134:137], v[130:133]
	v_mfma_f32_16x16x32_bf16 v[134:137], v[106:109], v[186:189], v[158:161]
	v_mfma_f32_16x16x32_bf16 v[154:157], v[118:121], v[190:193], v[154:157]
	v_mfma_f32_16x16x32_bf16 v[142:145], v[110:113], v[200:203], v[142:145]
	v_mfma_f32_16x16x32_bf16 v[138:141], v[118:121], v[200:203], v[138:141]
	v_mfma_f32_16x16x32_bf16 v[86:89], v[110:113], v[228:231], v[86:89]
	v_mfma_f32_16x16x32_bf16 v[74:77], v[118:121], v[228:231], v[74:77]
	v_mfma_f32_16x16x32_bf16 v[134:137], v[110:113], v[190:193], v[134:137]
	s_barrier
	ds_read_b128 v[158:161], v85 offset:16384
	ds_read_b128 v[170:173], v85 offset:17408
	ds_read_b128 v[186:189], v85 offset:18432
	ds_read_b128 v[190:193], v85 offset:19456
	ds_read_b128 v[196:199], v85 offset:20480
	ds_read_b128 v[200:203], v85 offset:21504
	ds_read_b128 v[208:211], v85 offset:22528
	ds_read_b128 v[228:231], v85 offset:23552
	s_add_i32 s28, s28, s50
	v_lshl_add_u64 v[204:205], s[34:35], 0, v[194:195]
	s_mov_b32 m0, s28
	s_nop 0
	global_load_lds_dwordx4 v[204:205], off
	s_add_i32 m0, s28, 0x2000
	s_add_u32 s28, s34, 0x80000
	v_lshl_add_u64 v[232:233], s[34:35], 0, v[2:3]
	s_addc_u32 s29, s35, 0
	s_add_i32 s33, s33, s50
	global_load_lds_dwordx4 v[232:233], off
	v_lshl_add_u64 v[234:235], s[28:29], 0, v[194:195]
	s_mov_b32 m0, s33
	v_lshl_add_u64 v[236:237], s[48:49], 0, v[6:7]
	global_load_lds_dwordx4 v[234:235], off
	v_lshl_add_u64 v[234:235], s[28:29], 0, v[2:3]
	s_add_i32 m0, s33, 0x2000
	s_nop 0
	global_load_lds_dwordx4 v[234:235], off
	v_lshl_add_u64 v[234:235], s[48:49], 0, v[4:5]
	s_mov_b32 m0, s51
	s_nop 0
	global_load_lds_dwordx4 v[234:235], off
	s_mov_b32 m0, s60
	s_nop 0
	global_load_lds_dwordx4 v[236:237], off
	s_waitcnt vmcnt(8)
	s_waitcnt lgkmcnt(0)
	s_barrier
; #define PG8_STAGE(bufoff, gbase, voff) do { _Pragma("unroll") for (int _i = 0; _i < 2; ++_i) \
;         __builtin_amdgcn_global_load_lds((const unsigned*)((const char*)(gbase) + (voff)[_i]), (LAS unsigned*)(lds + (bufoff) + ldsw + _i * 8192), 16, 0, 0); } while (0)
; #define PG8_LDA(dst, b, h) do { _Pragma("unroll") for (int m = 0; m < 4; ++m) _Pragma("unroll") for (int k = 0; k < 2; ++k) dst[m][k] = *(const LAS bf16x8*)(lds + PG8_SA(b, h) + aoff + m * 2048 + k * 1024); } while (0)
; #define PG8_LDB(dst, b, h) do { _Pragma("unroll") for (int n = 0; n < 2; ++n) _Pragma("unroll") for (int k = 0; k < 2; ++k) dst[n][k] = *(const LAS bf16x8*)(lds + PG8_SB(b, h) + boff + n * 2048 + k * 1024); } while (0)
; #define PG8_MMA(ai, bj, At, Bt) do { __builtin_amdgcn_s_setprio(1); _Pragma("unroll") for (int m = 0; m < 4; ++m) _Pragma("unroll") for (int n = 0; n < 2; ++n) _Pragma("unroll") for (int k = 0; k < 2; ++k) \
;         acc[ai][bj][m][n] = __builtin_amdgcn_mfma_f32_16x16x32_bf16(Bt[n][k], At[m][k], acc[ai][bj][m][n], 0, 0, 0); __builtin_amdgcn_s_setprio(0); } while (0)
; #define PG8_WAIT_V(n) asm volatile("s_waitcnt vmcnt(" #n ")" ::: "memory")
; #define PG8_WAIT_L(n) asm volatile("s_waitcnt lgkmcnt(" #n ")" ::: "memory")
; #define PG8_BAR __builtin_amdgcn_s_barrier()
; #define PG8_SCHED __builtin_amdgcn_sched_barrier(0)
; template <class Epi, class Sched, bool GATHER = false>
; __device__ __forceinline__ void gemm_phase(LAS unsigned char* lds, const int lda, const int ldb, const int K, const Sched& S, const Epi& E, const int* gidx = nullptr) {
;     ...
;             PG8_WAIT_V(8); PG8_WAIT_L(0); PG8_BAR; PG8_MMA(1, 0, At, B0); PG8_MMA(1, 1, At, B1); PG8_BAR; PG8_SCHED;
;             PG8_LDB(B0, 1, 0); PG8_LDB(B1, 1, 1); PG8_SCHED; PG8_LDA(At, 1, 0); PG8_STAGE(PG8_SA(0, 1), a2, o2[1]);
;             PG8_WAIT_V(8); PG8_WAIT_L(0); PG8_BAR; PG8_MMA(0, 0, At, B0); PG8_MMA(0, 1, At, B1); PG8_BAR; PG8_SCHED;
	v_mfma_f32_16x16x32_bf16 v[70:73], v[90:93], v[158:161], v[70:73]
	v_mfma_f32_16x16x32_bf16 v[66:69], v[98:101], v[158:161], v[66:69]
	v_mfma_f32_16x16x32_bf16 v[54:57], v[90:93], v[186:189], v[54:57]
	v_mfma_f32_16x16x32_bf16 v[46:49], v[98:101], v[186:189], v[46:49]
	v_mfma_f32_16x16x32_bf16 v[34:37], v[90:93], v[196:199], v[34:37]
	v_mfma_f32_16x16x32_bf16 v[26:29], v[98:101], v[196:199], v[26:29]
	v_mfma_f32_16x16x32_bf16 v[22:25], v[90:93], v[208:211], v[22:25]
	v_mfma_f32_16x16x32_bf16 v[18:21], v[98:101], v[208:211], v[18:21]
	v_mfma_f32_16x16x32_bf16 v[70:73], v[94:97], v[170:173], v[70:73]
	v_mfma_f32_16x16x32_bf16 v[66:69], v[102:105], v[170:173], v[66:69]
	v_mfma_f32_16x16x32_bf16 v[54:57], v[94:97], v[190:193], v[54:57]
	v_mfma_f32_16x16x32_bf16 v[46:49], v[102:105], v[190:193], v[46:49]
	v_mfma_f32_16x16x32_bf16 v[34:37], v[94:97], v[200:203], v[34:37]
	v_mfma_f32_16x16x32_bf16 v[26:29], v[102:105], v[200:203], v[26:29]
	v_mfma_f32_16x16x32_bf16 v[22:25], v[94:97], v[228:231], v[22:25]
	v_mfma_f32_16x16x32_bf16 v[18:21], v[102:105], v[228:231], v[18:21]
	v_mfma_f32_16x16x32_bf16 v[62:65], v[106:109], v[158:161], v[62:65]
	v_mfma_f32_16x16x32_bf16 v[58:61], v[114:117], v[158:161], v[58:61]
	v_mfma_f32_16x16x32_bf16 v[50:53], v[106:109], v[186:189], v[50:53]
	v_mfma_f32_16x16x32_bf16 v[42:45], v[114:117], v[186:189], v[42:45]
	v_mfma_f32_16x16x32_bf16 v[38:41], v[106:109], v[196:199], v[38:41]
	v_mfma_f32_16x16x32_bf16 v[30:33], v[114:117], v[196:199], v[30:33]
	v_mfma_f32_16x16x32_bf16 v[14:17], v[106:109], v[208:211], v[14:17]
	v_mfma_f32_16x16x32_bf16 v[10:13], v[114:117], v[208:211], v[10:13]
	v_mfma_f32_16x16x32_bf16 v[62:65], v[110:113], v[170:173], v[62:65]
	v_mfma_f32_16x16x32_bf16 v[58:61], v[118:121], v[170:173], v[58:61]
	v_mfma_f32_16x16x32_bf16 v[50:53], v[110:113], v[190:193], v[50:53]
	v_mfma_f32_16x16x32_bf16 v[42:45], v[118:121], v[190:193], v[42:45]
	v_mfma_f32_16x16x32_bf16 v[38:41], v[110:113], v[200:203], v[38:41]
	v_mfma_f32_16x16x32_bf16 v[30:33], v[118:121], v[200:203], v[30:33]
	v_mfma_f32_16x16x32_bf16 v[14:17], v[110:113], v[228:231], v[14:17]
	v_mfma_f32_16x16x32_bf16 v[10:13], v[118:121], v[228:231], v[10:13]
	s_barrier
	s_add_i32 s28, 0, 0x18000
	s_add_i32 s33, 0, 0x1c000
	v_add_u32_e32 v102, s28, v84
	v_add_u32_e32 v118, s33, v84
	ds_read_b128 v[90:93], v102
	ds_read_b128 v[94:97], v102 offset:1024
	ds_read_b128 v[98:101], v102 offset:2048
	ds_read_b128 v[102:105], v102 offset:3072
	ds_read_b128 v[106:109], v118
	ds_read_b128 v[110:113], v118 offset:1024
	ds_read_b128 v[114:117], v118 offset:2048
	ds_read_b128 v[118:121], v118 offset:3072
	ds_read_b128 v[158:161], v85 offset:32768
	ds_read_b128 v[170:173], v85 offset:33792
	ds_read_b128 v[186:189], v85 offset:34816
	ds_read_b128 v[190:193], v85 offset:35840
	ds_read_b128 v[196:199], v85 offset:36864
	ds_read_b128 v[200:203], v85 offset:37888
	ds_read_b128 v[208:211], v85 offset:38912
	ds_read_b128 v[228:231], v85 offset:39936
	s_mov_b32 m0, s66
	v_lshl_add_u64 v[238:239], s[48:49], 0, v[8:9]
	global_load_lds_dwordx4 v[238:239], off
	v_lshl_add_u64 v[238:239], s[48:49], 0, v[78:79]
	s_mov_b32 m0, s67
	s_nop 0
	global_load_lds_dwordx4 v[238:239], off
	s_waitcnt vmcnt(8)
	s_waitcnt lgkmcnt(0)
	s_barrier
	v_mfma_f32_16x16x32_bf16 v[182:185], v[90:93], v[158:161], v[182:185]
	v_mfma_f32_16x16x32_bf16 v[178:181], v[98:101], v[158:161], v[178:181]
	v_mfma_f32_16x16x32_bf16 v[166:169], v[90:93], v[186:189], v[166:169]
	v_mfma_f32_16x16x32_bf16 v[162:165], v[98:101], v[186:189], v[162:165]
	v_mfma_f32_16x16x32_bf16 v[150:153], v[90:93], v[196:199], v[150:153]
	v_mfma_f32_16x16x32_bf16 v[146:149], v[98:101], v[196:199], v[146:149]
	v_mfma_f32_16x16x32_bf16 v[126:129], v[90:93], v[208:211], v[126:129]
	v_mfma_f32_16x16x32_bf16 v[122:125], v[98:101], v[208:211], v[122:125]
	v_mfma_f32_16x16x32_bf16 v[182:185], v[94:97], v[170:173], v[182:185]
	v_mfma_f32_16x16x32_bf16 v[178:181], v[102:105], v[170:173], v[178:181]
	v_mfma_f32_16x16x32_bf16 v[166:169], v[94:97], v[190:193], v[166:169]
	v_mfma_f32_16x16x32_bf16 v[162:165], v[102:105], v[190:193], v[162:165]
	v_mfma_f32_16x16x32_bf16 v[150:153], v[94:97], v[200:203], v[150:153]
	v_mfma_f32_16x16x32_bf16 v[146:149], v[102:105], v[200:203], v[146:149]
	v_mfma_f32_16x16x32_bf16 v[126:129], v[94:97], v[228:231], v[126:129]
	v_mfma_f32_16x16x32_bf16 v[122:125], v[102:105], v[228:231], v[122:125]
	v_mfma_f32_16x16x32_bf16 v[174:177], v[106:109], v[158:161], v[174:177]
	v_mfma_f32_16x16x32_bf16 v[130:133], v[114:117], v[158:161], v[130:133]
	v_mfma_f32_16x16x32_bf16 v[174:177], v[110:113], v[170:173], v[174:177]
	v_mfma_f32_16x16x32_bf16 v[170:173], v[118:121], v[170:173], v[130:133]
	v_mfma_f32_16x16x32_bf16 v[130:133], v[106:109], v[186:189], v[134:137]
	v_mfma_f32_16x16x32_bf16 v[158:161], v[110:113], v[190:193], v[130:133]
	v_mfma_f32_16x16x32_bf16 v[130:133], v[114:117], v[186:189], v[154:157]
	v_mfma_f32_16x16x32_bf16 v[154:157], v[118:121], v[190:193], v[130:133]
	v_mfma_f32_16x16x32_bf16 v[130:133], v[106:109], v[196:199], v[142:145]
	v_mfma_f32_16x16x32_bf16 v[142:145], v[110:113], v[200:203], v[130:133]
	v_mfma_f32_16x16x32_bf16 v[130:133], v[114:117], v[196:199], v[138:141]
	v_mfma_f32_16x16x32_bf16 v[86:89], v[106:109], v[208:211], v[86:89]
	v_mfma_f32_16x16x32_bf16 v[74:77], v[114:117], v[208:211], v[74:77]
	v_mfma_f32_16x16x32_bf16 v[138:141], v[118:121], v[200:203], v[130:133]
	v_mfma_f32_16x16x32_bf16 v[86:89], v[110:113], v[228:231], v[86:89]
	v_mfma_f32_16x16x32_bf16 v[74:77], v[118:121], v[228:231], v[74:77]
	s_barrier
; #define PG8_STAGE(bufoff, gbase, voff) do { _Pragma("unroll") for (int _i = 0; _i < 2; ++_i) \
;         __builtin_amdgcn_global_load_lds((const unsigned*)((const char*)(gbase) + (voff)[_i]), (LAS unsigned*)(lds + (bufoff) + ldsw + _i * 8192), 16, 0, 0); } while (0)
; #define PG8_LDA(dst, b, h) do { _Pragma("unroll") for (int m = 0; m < 4; ++m) _Pragma("unroll") for (int k = 0; k < 2; ++k) dst[m][k] = *(const LAS bf16x8*)(lds + PG8_SA(b, h) + aoff + m * 2048 + k * 1024); } while (0)
; #define PG8_MMA(ai, bj, At, Bt) do { __builtin_amdgcn_s_setprio(1); _Pragma("unroll") for (int m = 0; m < 4; ++m) _Pragma("unroll") for (int n = 0; n < 2; ++n) _Pragma("unroll") for (int k = 0; k < 2; ++k) \
;         acc[ai][bj][m][n] = __builtin_amdgcn_mfma_f32_16x16x32_bf16(Bt[n][k], At[m][k], acc[ai][bj][m][n], 0, 0, 0); __builtin_amdgcn_s_setprio(0); } while (0)
; #define PG8_WAIT_V(n) asm volatile("s_waitcnt vmcnt(" #n ")" ::: "memory")
; #define PG8_WAIT_L(n) asm volatile("s_waitcnt lgkmcnt(" #n ")" ::: "memory")
; #define PG8_BAR __builtin_amdgcn_s_barrier()
; #define PG8_SCHED __builtin_amdgcn_sched_barrier(0)
; template <class Epi, class Sched, bool GATHER = false>
; __device__ __forceinline__ void gemm_phase(LAS unsigned char* lds, const int lda, const int ldb, const int K, const Sched& S, const Epi& E, const int* gidx = nullptr) {
;     ...
;             PG8_LDA(At, 1, 1); PG8_STAGE(PG8_SB(1, 0), b3, voffB); PG8_STAGE(PG8_SB(1, 1), b3 + hstepB, voffB); PG8_STAGE(PG8_SA(1, 0), a3, o2[0]);
;             PG8_WAIT_V(8); PG8_WAIT_L(0); PG8_BAR; PG8_MMA(1, 0, At, B0); PG8_MMA(1, 1, At, B1); PG8_BAR; PG8_SCHED;
;         }
;         if (wr == 0) PG8_BAR;
	ds_read_b128 v[130:133], v85 offset:49152
	ds_read_b128 v[134:137], v85 offset:50176
	ds_read_b128 v[186:189], v85 offset:51200
	ds_read_b128 v[190:193], v85 offset:52224
	ds_read_b128 v[196:199], v85 offset:53248
	ds_read_b128 v[200:203], v85 offset:54272
	ds_read_b128 v[208:211], v85 offset:55296
	ds_read_b128 v[228:231], v85 offset:56320
	s_add_i32 s28, s28, s50
	v_lshl_add_u64 v[204:205], v[204:205], 0, s[64:65]
	s_mov_b32 m0, s28
	s_nop 0
	global_load_lds_dwordx4 v[204:205], off
	s_add_i32 m0, s28, 0x2000
	s_add_u32 s28, s34, 0x80080
	v_lshl_add_u64 v[204:205], v[232:233], 0, s[64:65]
	s_addc_u32 s29, s35, 0
	s_add_i32 s33, s33, s50
	global_load_lds_dwordx4 v[204:205], off
	v_lshl_add_u64 v[204:205], s[28:29], 0, v[194:195]
	s_mov_b32 m0, s33
	s_nop 0
	global_load_lds_dwordx4 v[204:205], off
	v_lshl_add_u64 v[204:205], s[28:29], 0, v[2:3]
	s_add_i32 m0, s33, 0x2000
	s_nop 0
	global_load_lds_dwordx4 v[204:205], off
	v_lshl_add_u64 v[204:205], v[234:235], 0, s[64:65]
	s_mov_b32 m0, s70
	s_nop 0
	global_load_lds_dwordx4 v[204:205], off
	v_lshl_add_u64 v[204:205], v[236:237], 0, s[64:65]
	s_mov_b32 m0, s71
	s_nop 0
	global_load_lds_dwordx4 v[204:205], off
	s_waitcnt vmcnt(8)
	s_waitcnt lgkmcnt(0)
	s_barrier
	v_mfma_f32_16x16x32_bf16 v[70:73], v[90:93], v[130:133], v[70:73]
	v_mfma_f32_16x16x32_bf16 v[66:69], v[98:101], v[130:133], v[66:69]
	v_mfma_f32_16x16x32_bf16 v[54:57], v[90:93], v[186:189], v[54:57]
	v_mfma_f32_16x16x32_bf16 v[46:49], v[98:101], v[186:189], v[46:49]
	v_mfma_f32_16x16x32_bf16 v[34:37], v[90:93], v[196:199], v[34:37]
	v_mfma_f32_16x16x32_bf16 v[26:29], v[98:101], v[196:199], v[26:29]
	v_mfma_f32_16x16x32_bf16 v[22:25], v[90:93], v[208:211], v[22:25]
	v_mfma_f32_16x16x32_bf16 v[18:21], v[98:101], v[208:211], v[18:21]
	v_mfma_f32_16x16x32_bf16 v[70:73], v[94:97], v[134:137], v[70:73]
	v_mfma_f32_16x16x32_bf16 v[66:69], v[102:105], v[134:137], v[66:69]
	v_mfma_f32_16x16x32_bf16 v[54:57], v[94:97], v[190:193], v[54:57]
	v_mfma_f32_16x16x32_bf16 v[46:49], v[102:105], v[190:193], v[46:49]
	v_mfma_f32_16x16x32_bf16 v[34:37], v[94:97], v[200:203], v[34:37]
	v_mfma_f32_16x16x32_bf16 v[26:29], v[102:105], v[200:203], v[26:29]
	v_mfma_f32_16x16x32_bf16 v[22:25], v[94:97], v[228:231], v[22:25]
	v_mfma_f32_16x16x32_bf16 v[18:21], v[102:105], v[228:231], v[18:21]
	v_mfma_f32_16x16x32_bf16 v[62:65], v[106:109], v[130:133], v[62:65]
	v_mfma_f32_16x16x32_bf16 v[58:61], v[114:117], v[130:133], v[58:61]
	v_mfma_f32_16x16x32_bf16 v[50:53], v[106:109], v[186:189], v[50:53]
	v_mfma_f32_16x16x32_bf16 v[42:45], v[114:117], v[186:189], v[42:45]
	v_mfma_f32_16x16x32_bf16 v[38:41], v[106:109], v[196:199], v[38:41]
	v_mfma_f32_16x16x32_bf16 v[30:33], v[114:117], v[196:199], v[30:33]
	v_mfma_f32_16x16x32_bf16 v[14:17], v[106:109], v[208:211], v[14:17]
	v_mfma_f32_16x16x32_bf16 v[10:13], v[114:117], v[208:211], v[10:13]
	v_mfma_f32_16x16x32_bf16 v[62:65], v[110:113], v[134:137], v[62:65]
	v_mfma_f32_16x16x32_bf16 v[58:61], v[118:121], v[134:137], v[58:61]
	v_mfma_f32_16x16x32_bf16 v[50:53], v[110:113], v[190:193], v[50:53]
	v_mfma_f32_16x16x32_bf16 v[42:45], v[118:121], v[190:193], v[42:45]
	v_mfma_f32_16x16x32_bf16 v[38:41], v[110:113], v[200:203], v[38:41]
	v_mfma_f32_16x16x32_bf16 v[30:33], v[118:121], v[200:203], v[30:33]
	v_mfma_f32_16x16x32_bf16 v[14:17], v[110:113], v[228:231], v[14:17]
	v_mfma_f32_16x16x32_bf16 v[10:13], v[118:121], v[228:231], v[10:13]
	s_barrier
	s_add_i32 s72, s72, 2
	s_add_u32 s12, s12, 0x100
	s_addc_u32 s13, s13, 0
	s_cmp_gt_u32 s72, 29
	s_cbranch_scc0 .LBB0_1186
	s_cmpk_lt_u32 s8, 0x100
	s_cbranch_scc0 .LBB0_1189
	s_barrier

; #define PG8_AOFF(of, u) do { _Pragma("unroll") for (int hh_ = 0; hh_ < 2; ++hh_) _Pragma("unroll") for (int i_ = 0; i_ < 2; ++i_) { \
;         if constexpr (GATHER) of[hh_][i_] = (unsigned)gidx[(u).pm * 256 + hh_ * 128 + RA[i_]] * (unsigned)(lda * 2) + CA2[i_]; \
;         else of[hh_][i_] = (unsigned)((hh_ * HALF + RA[i_]) * lda) * 2u + CA2[i_]; } } while (0)
; #define PG8_STAGE(bufoff, gbase, voff) do { _Pragma("unroll") for (int _i = 0; _i < 2; ++_i) \
;         __builtin_amdgcn_global_load_lds((const unsigned*)((const char*)(gbase) + (voff)[_i]), (LAS unsigned*)(lds + (bufoff) + ldsw + _i * 8192), 16, 0, 0); } while (0)
; #define PG8_LDA(dst, b, h) do { _Pragma("unroll") for (int m = 0; m < 4; ++m) _Pragma("unroll") for (int k = 0; k < 2; ++k) dst[m][k] = *(const LAS bf16x8*)(lds + PG8_SA(b, h) + aoff + m * 2048 + k * 1024); } while (0)
; #define PG8_WAIT_V(n) asm volatile("s_waitcnt vmcnt(" #n ")" ::: "memory")
; #define PG8_WAIT_L(n) asm volatile("s_waitcnt lgkmcnt(" #n ")" ::: "memory")
; template <class Epi, class Sched, bool GATHER = false>
; __device__ __forceinline__ void gemm_phase(LAS unsigned char* lds, const int lda, const int ldb, const int K, const Sched& S, const Epi& E, const int* gidx = nullptr) {
;     ...
;             const bool last = (t == nt - 2);
;             if constexpr (GATHER) { if (last && has_next) PG8_AOFF(ofn, nxt); }
;             const char* a1 = cA + (size_t)(t + 1) * kstep;
;             const char* a2 = last ? nA : cA + (size_t)(t + 2) * kstep; const char* b2 = last ? nB : cB + (size_t)(t + 2) * kstep;
;             const char* a3 = a2 + kstep; const char* b3 = b2 + kstep;
;             unsigned o2[2][2];
; #pragma unroll
;             for (int hh = 0; hh < 2; ++hh)
; #pragma unroll
;                 for (int i = 0; i < 2; ++i) { if constexpr (GATHER) o2[hh][i] = last ? ofn[hh][i] : ofc[hh][i]; else o2[hh][i] = ofc[hh][i]; }
;             PG8_LDB(B0, 0, 0); PG8_LDB(B1, 0, 1); PG8_SCHED; PG8_LDA(At, 0, 0); PG8_STAGE(PG8_SA(1, 1), a1, ofc[1]);
;             PG8_WAIT_V(8); PG8_WAIT_L(0); PG8_BAR; PG8_MMA(0, 0, At, B0); PG8_MMA(0, 1, At, B1); PG8_BAR; PG8_SCHED;
;             PG8_LDA(At, 0, 1); PG8_STAGE(PG8_SB(0, 0), b2, voffB); PG8_STAGE(PG8_SB(0, 1), b2 + hstepB, voffB); PG8_STAGE(PG8_SA(0, 0), a2, o2[0]);
;             PG8_WAIT_V(8); PG8_WAIT_L(0); PG8_BAR; PG8_MMA(1, 0, At, B0); PG8_MMA(1, 1, At, B1); PG8_BAR; PG8_SCHED;
.LBB0_1666:
	s_add_i32 s28, 0, 0x10000
	v_add_u32_e32 v135, s28, v159
	s_add_i32 s33, 0, 0x14000
	ds_read_b128 v[164:167], v135
	ds_read_b128 v[168:171], v135 offset:1024
	ds_read_b128 v[172:175], v135 offset:2048
	ds_read_b128 v[176:179], v135 offset:3072
	v_add_u32_e32 v135, s33, v159
	ds_read_b128 v[180:183], v135
	ds_read_b128 v[184:187], v135 offset:1024
	ds_read_b128 v[188:191], v135 offset:2048
	ds_read_b128 v[196:199], v135 offset:3072
	v_cndmask_b32_e64 v194, v138, v141, s[34:35]
	v_cndmask_b32_e64 v192, v136, v143, s[34:35]
	v_cndmask_b32_e64 v135, v140, v161, s[34:35]
	v_cndmask_b32_e64 v137, v142, v162, s[34:35]
	ds_read_b128 v[200:203], v160
	ds_read_b128 v[204:207], v160 offset:1024
	ds_read_b128 v[208:211], v160 offset:2048
	ds_read_b128 v[228:231], v160 offset:3072
	ds_read_b128 v[232:235], v160 offset:4096
	ds_read_b128 v[236:239], v160 offset:5120
	ds_read_b128 v[240:243], v160 offset:6144
	ds_read_b128 v[244:247], v160 offset:7168
	v_lshl_add_u64 v[222:223], v[154:155], 0, s[44:45]
	s_add_i32 m0, s10, 0xc000
	s_add_u32 s12, s26, s44
	s_addc_u32 s13, s27, s45
	s_add_u32 s28, s12, 0x24400100
	s_addc_u32 s29, s13, 0
	s_and_b64 s[12:13], s[34:35], exec
	s_cselect_b32 s49, s17, s29
	s_cselect_b32 s48, s16, s28
	s_add_u32 s28, s72, s44
	s_addc_u32 s29, s73, s45
	s_and_b64 s[12:13], s[34:35], exec
	s_cselect_b32 s13, s41, s29
	s_cselect_b32 s12, s40, s28
	s_add_i32 s28, 0, 0x10000
	global_load_lds_dwordx4 v[222:223], off
	v_lshl_add_u64 v[222:223], v[152:153], 0, s[44:45]
	s_add_i32 m0, s10, 0xe000
	s_nop 0
	global_load_lds_dwordx4 v[222:223], off
	s_waitcnt vmcnt(8)
	s_waitcnt lgkmcnt(0)
	s_barrier
	v_mfma_f32_16x16x32_bf16 v[126:129], v[164:167], v[200:203], v[126:129]
	v_mfma_f32_16x16x32_bf16 v[118:121], v[172:175], v[200:203], v[118:121]
	v_mfma_f32_16x16x32_bf16 v[110:113], v[164:167], v[208:211], v[110:113]
	v_mfma_f32_16x16x32_bf16 v[102:105], v[172:175], v[208:211], v[102:105]
	v_mfma_f32_16x16x32_bf16 v[94:97], v[164:167], v[232:235], v[94:97]
	v_mfma_f32_16x16x32_bf16 v[86:89], v[172:175], v[232:235], v[86:89]
	v_mfma_f32_16x16x32_bf16 v[78:81], v[164:167], v[240:243], v[78:81]
	v_mfma_f32_16x16x32_bf16 v[70:73], v[172:175], v[240:243], v[70:73]
	v_mfma_f32_16x16x32_bf16 v[126:129], v[168:171], v[204:207], v[126:129]
	v_mfma_f32_16x16x32_bf16 v[118:121], v[176:179], v[204:207], v[118:121]
	v_mfma_f32_16x16x32_bf16 v[110:113], v[168:171], v[228:231], v[110:113]
	v_mfma_f32_16x16x32_bf16 v[102:105], v[176:179], v[228:231], v[102:105]
	v_mfma_f32_16x16x32_bf16 v[94:97], v[168:171], v[236:239], v[94:97]
	v_mfma_f32_16x16x32_bf16 v[86:89], v[176:179], v[236:239], v[86:89]
	v_mfma_f32_16x16x32_bf16 v[78:81], v[168:171], v[244:247], v[78:81]
	v_mfma_f32_16x16x32_bf16 v[70:73], v[176:179], v[244:247], v[70:73]
	v_mfma_f32_16x16x32_bf16 v[122:125], v[180:183], v[200:203], v[122:125]
	v_mfma_f32_16x16x32_bf16 v[114:117], v[188:191], v[200:203], v[114:117]
	v_mfma_f32_16x16x32_bf16 v[106:109], v[180:183], v[208:211], v[106:109]
	v_mfma_f32_16x16x32_bf16 v[98:101], v[188:191], v[208:211], v[98:101]
	v_mfma_f32_16x16x32_bf16 v[90:93], v[180:183], v[232:235], v[90:93]
	v_mfma_f32_16x16x32_bf16 v[82:85], v[188:191], v[232:235], v[82:85]
	v_mfma_f32_16x16x32_bf16 v[74:77], v[180:183], v[240:243], v[74:77]
	v_mfma_f32_16x16x32_bf16 v[66:69], v[188:191], v[240:243], v[66:69]
	v_mfma_f32_16x16x32_bf16 v[122:125], v[184:187], v[204:207], v[122:125]
	v_mfma_f32_16x16x32_bf16 v[114:117], v[196:199], v[204:207], v[114:117]
	v_mfma_f32_16x16x32_bf16 v[106:109], v[184:187], v[228:231], v[106:109]
	v_mfma_f32_16x16x32_bf16 v[98:101], v[196:199], v[228:231], v[98:101]
	v_mfma_f32_16x16x32_bf16 v[90:93], v[184:187], v[236:239], v[90:93]
	v_mfma_f32_16x16x32_bf16 v[82:85], v[196:199], v[236:239], v[82:85]
	v_mfma_f32_16x16x32_bf16 v[74:77], v[184:187], v[244:247], v[74:77]
	v_mfma_f32_16x16x32_bf16 v[66:69], v[196:199], v[244:247], v[66:69]
	s_barrier
	ds_read_b128 v[200:203], v160 offset:16384
	ds_read_b128 v[204:207], v160 offset:17408
	ds_read_b128 v[208:211], v160 offset:18432
	ds_read_b128 v[228:231], v160 offset:19456
	ds_read_b128 v[232:235], v160 offset:20480
	ds_read_b128 v[236:239], v160 offset:21504
	ds_read_b128 v[240:243], v160 offset:22528
	ds_read_b128 v[244:247], v160 offset:23552
	s_add_i32 s28, s28, s9
	v_lshl_add_u64 v[222:223], s[12:13], 0, v[130:131]
	s_mov_b32 m0, s28
	s_nop 0
	global_load_lds_dwordx4 v[222:223], off
	s_add_i32 m0, s28, 0x2000
	s_add_u32 s28, s12, 0x80000
	v_lshl_add_u64 v[224:225], s[12:13], 0, v[132:133]
	s_addc_u32 s29, s13, 0
	s_add_i32 s33, s33, s9
	global_load_lds_dwordx4 v[224:225], off
	v_lshl_add_u64 v[214:215], s[28:29], 0, v[130:131]
	s_mov_b32 m0, s33
	v_mov_b32_e32 v193, v195
	global_load_lds_dwordx4 v[214:215], off
	v_lshl_add_u64 v[214:215], s[28:29], 0, v[132:133]
	s_add_i32 m0, s33, 0x2000
	s_nop 0
	global_load_lds_dwordx4 v[214:215], off
	s_mov_b32 m0, s10
	v_lshl_add_u64 v[214:215], s[48:49], 0, v[194:195]
	global_load_lds_dwordx4 v194, s[48:49]
	s_mov_b32 m0, s11
	s_nop 0
	global_load_lds_dwordx4 v192, s[48:49]
	s_waitcnt vmcnt(8)
	s_waitcnt lgkmcnt(0)
	v_lshl_add_u64 v[192:193], s[48:49], 0, v[192:193]
	s_barrier
; #define PG8_STAGE(bufoff, gbase, voff) do { _Pragma("unroll") for (int _i = 0; _i < 2; ++_i) \
;         __builtin_amdgcn_global_load_lds((const unsigned*)((const char*)(gbase) + (voff)[_i]), (LAS unsigned*)(lds + (bufoff) + ldsw + _i * 8192), 16, 0, 0); } while (0)
; #define PG8_LDA(dst, b, h) do { _Pragma("unroll") for (int m = 0; m < 4; ++m) _Pragma("unroll") for (int k = 0; k < 2; ++k) dst[m][k] = *(const LAS bf16x8*)(lds + PG8_SA(b, h) + aoff + m * 2048 + k * 1024); } while (0)
; #define PG8_LDB(dst, b, h) do { _Pragma("unroll") for (int n = 0; n < 2; ++n) _Pragma("unroll") for (int k = 0; k < 2; ++k) dst[n][k] = *(const LAS bf16x8*)(lds + PG8_SB(b, h) + boff + n * 2048 + k * 1024); } while (0)
; #define PG8_MMA(ai, bj, At, Bt) do { __builtin_amdgcn_s_setprio(1); _Pragma("unroll") for (int m = 0; m < 4; ++m) _Pragma("unroll") for (int n = 0; n < 2; ++n) _Pragma("unroll") for (int k = 0; k < 2; ++k) \
;         acc[ai][bj][m][n] = __builtin_amdgcn_mfma_f32_16x16x32_bf16(Bt[n][k], At[m][k], acc[ai][bj][m][n], 0, 0, 0); __builtin_amdgcn_s_setprio(0); } while (0)
; #define PG8_WAIT_V(n) asm volatile("s_waitcnt vmcnt(" #n ")" ::: "memory")
; #define PG8_WAIT_L(n) asm volatile("s_waitcnt lgkmcnt(" #n ")" ::: "memory")
; #define PG8_BAR __builtin_amdgcn_s_barrier()
; #define PG8_SCHED __builtin_amdgcn_sched_barrier(0)
; template <class Epi, class Sched, bool GATHER = false>
; __device__ __forceinline__ void gemm_phase(LAS unsigned char* lds, const int lda, const int ldb, const int K, const Sched& S, const Epi& E, const int* gidx = nullptr) {
;     ...
;             PG8_WAIT_V(8); PG8_WAIT_L(0); PG8_BAR; PG8_MMA(1, 0, At, B0); PG8_MMA(1, 1, At, B1); PG8_BAR; PG8_SCHED;
;             PG8_LDB(B0, 1, 0); PG8_LDB(B1, 1, 1); PG8_SCHED; PG8_LDA(At, 1, 0); PG8_STAGE(PG8_SA(0, 1), a2, o2[1]);
;             PG8_WAIT_V(8); PG8_WAIT_L(0); PG8_BAR; PG8_MMA(0, 0, At, B0); PG8_MMA(0, 1, At, B1); PG8_BAR; PG8_SCHED;
	v_mfma_f32_16x16x32_bf16 v[62:65], v[164:167], v[200:203], v[62:65]
	v_mfma_f32_16x16x32_bf16 v[54:57], v[172:175], v[200:203], v[54:57]
	v_mfma_f32_16x16x32_bf16 v[46:49], v[164:167], v[208:211], v[46:49]
	v_mfma_f32_16x16x32_bf16 v[38:41], v[172:175], v[208:211], v[38:41]
	v_mfma_f32_16x16x32_bf16 v[22:25], v[164:167], v[232:235], v[22:25]
	v_mfma_f32_16x16x32_bf16 v[18:21], v[172:175], v[232:235], v[18:21]
	v_mfma_f32_16x16x32_bf16 v[6:9], v[164:167], v[240:243], v[6:9]
	v_mfma_f32_16x16x32_bf16 v[2:5], v[172:175], v[240:243], v[2:5]
	v_mfma_f32_16x16x32_bf16 v[62:65], v[168:171], v[204:207], v[62:65]
	v_mfma_f32_16x16x32_bf16 v[54:57], v[176:179], v[204:207], v[54:57]
	v_mfma_f32_16x16x32_bf16 v[46:49], v[168:171], v[228:231], v[46:49]
	v_mfma_f32_16x16x32_bf16 v[38:41], v[176:179], v[228:231], v[38:41]
	v_mfma_f32_16x16x32_bf16 v[22:25], v[168:171], v[236:239], v[22:25]
	v_mfma_f32_16x16x32_bf16 v[18:21], v[176:179], v[236:239], v[18:21]
	v_mfma_f32_16x16x32_bf16 v[6:9], v[168:171], v[244:247], v[6:9]
	v_mfma_f32_16x16x32_bf16 v[2:5], v[176:179], v[244:247], v[2:5]
	v_mfma_f32_16x16x32_bf16 v[58:61], v[180:183], v[200:203], v[58:61]
	v_mfma_f32_16x16x32_bf16 v[50:53], v[188:191], v[200:203], v[50:53]
	v_mfma_f32_16x16x32_bf16 v[42:45], v[180:183], v[208:211], v[42:45]
	v_mfma_f32_16x16x32_bf16 v[34:37], v[188:191], v[208:211], v[34:37]
	v_mfma_f32_16x16x32_bf16 v[30:33], v[180:183], v[232:235], v[30:33]
	v_mfma_f32_16x16x32_bf16 v[26:29], v[188:191], v[232:235], v[26:29]
	v_mfma_f32_16x16x32_bf16 v[14:17], v[180:183], v[240:243], v[14:17]
	v_mfma_f32_16x16x32_bf16 v[10:13], v[188:191], v[240:243], v[10:13]
	v_mfma_f32_16x16x32_bf16 v[58:61], v[184:187], v[204:207], v[58:61]
	v_mfma_f32_16x16x32_bf16 v[50:53], v[196:199], v[204:207], v[50:53]
	v_mfma_f32_16x16x32_bf16 v[42:45], v[184:187], v[228:231], v[42:45]
	v_mfma_f32_16x16x32_bf16 v[34:37], v[196:199], v[228:231], v[34:37]
	v_mfma_f32_16x16x32_bf16 v[30:33], v[184:187], v[236:239], v[30:33]
	v_mfma_f32_16x16x32_bf16 v[26:29], v[196:199], v[236:239], v[26:29]
	v_mfma_f32_16x16x32_bf16 v[14:17], v[184:187], v[244:247], v[14:17]
	v_mfma_f32_16x16x32_bf16 v[10:13], v[196:199], v[244:247], v[10:13]
	s_barrier
	s_add_i32 s28, 0, 0x18000
	v_add_u32_e32 v163, s28, v159
	s_add_i32 s29, 0, 0x1c000
	ds_read_b128 v[164:167], v163
	ds_read_b128 v[168:171], v163 offset:1024
	ds_read_b128 v[172:175], v163 offset:2048
	ds_read_b128 v[176:179], v163 offset:3072
	v_add_u32_e32 v163, s29, v159
	ds_read_b128 v[180:183], v163
	ds_read_b128 v[184:187], v163 offset:1024
	ds_read_b128 v[188:191], v163 offset:2048
	ds_read_b128 v[196:199], v163 offset:3072
	ds_read_b128 v[200:203], v160 offset:32768
	ds_read_b128 v[204:207], v160 offset:33792
	ds_read_b128 v[208:211], v160 offset:34816
	ds_read_b128 v[228:231], v160 offset:35840
	ds_read_b128 v[232:235], v160 offset:36864
	ds_read_b128 v[236:239], v160 offset:37888
	ds_read_b128 v[240:243], v160 offset:38912
	ds_read_b128 v[244:247], v160 offset:39936
	s_mov_b32 m0, s22
	s_nop 0
	global_load_lds_dwordx4 v135, s[48:49]
	s_mov_b32 m0, s23
	s_nop 0
	global_load_lds_dwordx4 v137, s[48:49]
	s_waitcnt vmcnt(8)
	s_waitcnt lgkmcnt(0)
	s_barrier
	v_mfma_f32_16x16x32_bf16 v[126:129], v[164:167], v[200:203], v[126:129]
	v_mfma_f32_16x16x32_bf16 v[118:121], v[172:175], v[200:203], v[118:121]
	v_mfma_f32_16x16x32_bf16 v[110:113], v[164:167], v[208:211], v[110:113]
	v_mfma_f32_16x16x32_bf16 v[102:105], v[172:175], v[208:211], v[102:105]
	v_mfma_f32_16x16x32_bf16 v[94:97], v[164:167], v[232:235], v[94:97]
	v_mfma_f32_16x16x32_bf16 v[86:89], v[172:175], v[232:235], v[86:89]
	v_mfma_f32_16x16x32_bf16 v[78:81], v[164:167], v[240:243], v[78:81]
	v_mfma_f32_16x16x32_bf16 v[70:73], v[172:175], v[240:243], v[70:73]
	v_mfma_f32_16x16x32_bf16 v[126:129], v[168:171], v[204:207], v[126:129]
	v_mfma_f32_16x16x32_bf16 v[118:121], v[176:179], v[204:207], v[118:121]
	v_mfma_f32_16x16x32_bf16 v[110:113], v[168:171], v[228:231], v[110:113]
	v_mfma_f32_16x16x32_bf16 v[102:105], v[176:179], v[228:231], v[102:105]
	v_mfma_f32_16x16x32_bf16 v[94:97], v[168:171], v[236:239], v[94:97]
	v_mfma_f32_16x16x32_bf16 v[86:89], v[176:179], v[236:239], v[86:89]
	v_mfma_f32_16x16x32_bf16 v[78:81], v[168:171], v[244:247], v[78:81]
	v_mfma_f32_16x16x32_bf16 v[70:73], v[176:179], v[244:247], v[70:73]
	v_mfma_f32_16x16x32_bf16 v[122:125], v[180:183], v[200:203], v[122:125]
	v_mfma_f32_16x16x32_bf16 v[114:117], v[188:191], v[200:203], v[114:117]
	v_mfma_f32_16x16x32_bf16 v[106:109], v[180:183], v[208:211], v[106:109]
	v_mfma_f32_16x16x32_bf16 v[98:101], v[188:191], v[208:211], v[98:101]
	v_mfma_f32_16x16x32_bf16 v[90:93], v[180:183], v[232:235], v[90:93]
	v_mfma_f32_16x16x32_bf16 v[82:85], v[188:191], v[232:235], v[82:85]
	v_mfma_f32_16x16x32_bf16 v[74:77], v[180:183], v[240:243], v[74:77]
	v_mfma_f32_16x16x32_bf16 v[66:69], v[188:191], v[240:243], v[66:69]
	v_mfma_f32_16x16x32_bf16 v[122:125], v[184:187], v[204:207], v[122:125]
	v_mfma_f32_16x16x32_bf16 v[114:117], v[196:199], v[204:207], v[114:117]
	v_mfma_f32_16x16x32_bf16 v[106:109], v[184:187], v[228:231], v[106:109]
	v_mfma_f32_16x16x32_bf16 v[98:101], v[196:199], v[228:231], v[98:101]
	v_mfma_f32_16x16x32_bf16 v[90:93], v[184:187], v[236:239], v[90:93]
	v_mfma_f32_16x16x32_bf16 v[82:85], v[196:199], v[236:239], v[82:85]
	v_mfma_f32_16x16x32_bf16 v[74:77], v[184:187], v[244:247], v[74:77]
	v_mfma_f32_16x16x32_bf16 v[66:69], v[196:199], v[244:247], v[66:69]
	s_barrier
; #define PG8_STAGE(bufoff, gbase, voff) do { _Pragma("unroll") for (int _i = 0; _i < 2; ++_i) \
;         __builtin_amdgcn_global_load_lds((const unsigned*)((const char*)(gbase) + (voff)[_i]), (LAS unsigned*)(lds + (bufoff) + ldsw + _i * 8192), 16, 0, 0); } while (0)
; #define PG8_LDA(dst, b, h) do { _Pragma("unroll") for (int m = 0; m < 4; ++m) _Pragma("unroll") for (int k = 0; k < 2; ++k) dst[m][k] = *(const LAS bf16x8*)(lds + PG8_SA(b, h) + aoff + m * 2048 + k * 1024); } while (0)
; #define PG8_MMA(ai, bj, At, Bt) do { __builtin_amdgcn_s_setprio(1); _Pragma("unroll") for (int m = 0; m < 4; ++m) _Pragma("unroll") for (int n = 0; n < 2; ++n) _Pragma("unroll") for (int k = 0; k < 2; ++k) \
;         acc[ai][bj][m][n] = __builtin_amdgcn_mfma_f32_16x16x32_bf16(Bt[n][k], At[m][k], acc[ai][bj][m][n], 0, 0, 0); __builtin_amdgcn_s_setprio(0); } while (0)
; #define PG8_WAIT_V(n) asm volatile("s_waitcnt vmcnt(" #n ")" ::: "memory")
; #define PG8_WAIT_L(n) asm volatile("s_waitcnt lgkmcnt(" #n ")" ::: "memory")
; #define PG8_BAR __builtin_amdgcn_s_barrier()
; #define PG8_SCHED __builtin_amdgcn_sched_barrier(0)
; template <class Epi, class Sched, bool GATHER = false>
; __device__ __forceinline__ void gemm_phase(LAS unsigned char* lds, const int lda, const int ldb, const int K, const Sched& S, const Epi& E, const int* gidx = nullptr) {
;     ...
;             PG8_LDA(At, 1, 1); PG8_STAGE(PG8_SB(1, 0), b3, voffB); PG8_STAGE(PG8_SB(1, 1), b3 + hstepB, voffB); PG8_STAGE(PG8_SA(1, 0), a3, o2[0]);
;             PG8_WAIT_V(8); PG8_WAIT_L(0); PG8_BAR; PG8_MMA(1, 0, At, B0); PG8_MMA(1, 1, At, B1); PG8_BAR; PG8_SCHED;
;         }
	ds_read_b128 v[200:203], v160 offset:49152
	ds_read_b128 v[204:207], v160 offset:50176
	ds_read_b128 v[208:211], v160 offset:51200
	ds_read_b128 v[228:231], v160 offset:52224
	ds_read_b128 v[232:235], v160 offset:53248
	ds_read_b128 v[236:239], v160 offset:54272
	ds_read_b128 v[240:243], v160 offset:55296
	ds_read_b128 v[244:247], v160 offset:56320
	s_add_i32 s28, s28, s9
	v_lshl_add_u64 v[222:223], v[222:223], 0, s[64:65]
	s_mov_b32 m0, s28
	s_nop 0
	global_load_lds_dwordx4 v[222:223], off
	s_add_i32 m0, s28, 0x2000
	s_add_u32 s12, s12, 0x80080
	v_lshl_add_u64 v[222:223], v[224:225], 0, s[64:65]
	s_addc_u32 s13, s13, 0
	s_add_i32 s28, s29, s9
	global_load_lds_dwordx4 v[222:223], off
	v_lshl_add_u64 v[222:223], s[12:13], 0, v[130:131]
	s_mov_b32 m0, s28
	v_lshl_add_u64 v[214:215], v[214:215], 0, s[64:65]
	global_load_lds_dwordx4 v[222:223], off
	v_lshl_add_u64 v[222:223], s[12:13], 0, v[132:133]
	s_add_i32 m0, s28, 0x2000
	v_lshl_add_u64 v[192:193], v[192:193], 0, s[64:65]
	global_load_lds_dwordx4 v[222:223], off
	s_mov_b32 m0, s50
	s_nop 0
	global_load_lds_dwordx4 v[214:215], off
	s_mov_b32 m0, s51
	s_nop 0
	global_load_lds_dwordx4 v[192:193], off
	s_waitcnt vmcnt(8)
	s_waitcnt lgkmcnt(0)
	s_barrier
	v_mfma_f32_16x16x32_bf16 v[62:65], v[164:167], v[200:203], v[62:65]
	v_mfma_f32_16x16x32_bf16 v[54:57], v[172:175], v[200:203], v[54:57]
	v_mfma_f32_16x16x32_bf16 v[46:49], v[164:167], v[208:211], v[46:49]
	v_mfma_f32_16x16x32_bf16 v[38:41], v[172:175], v[208:211], v[38:41]
	v_mfma_f32_16x16x32_bf16 v[22:25], v[164:167], v[232:235], v[22:25]
	v_mfma_f32_16x16x32_bf16 v[18:21], v[172:175], v[232:235], v[18:21]
	v_mfma_f32_16x16x32_bf16 v[6:9], v[164:167], v[240:243], v[6:9]
	v_mfma_f32_16x16x32_bf16 v[2:5], v[172:175], v[240:243], v[2:5]
	v_mfma_f32_16x16x32_bf16 v[62:65], v[168:171], v[204:207], v[62:65]
	v_mfma_f32_16x16x32_bf16 v[54:57], v[176:179], v[204:207], v[54:57]
	v_mfma_f32_16x16x32_bf16 v[46:49], v[168:171], v[228:231], v[46:49]
	v_mfma_f32_16x16x32_bf16 v[38:41], v[176:179], v[228:231], v[38:41]
	v_mfma_f32_16x16x32_bf16 v[22:25], v[168:171], v[236:239], v[22:25]
	v_mfma_f32_16x16x32_bf16 v[18:21], v[176:179], v[236:239], v[18:21]
	v_mfma_f32_16x16x32_bf16 v[6:9], v[168:171], v[244:247], v[6:9]
	v_mfma_f32_16x16x32_bf16 v[2:5], v[176:179], v[244:247], v[2:5]
	v_mfma_f32_16x16x32_bf16 v[58:61], v[180:183], v[200:203], v[58:61]
	v_mfma_f32_16x16x32_bf16 v[50:53], v[188:191], v[200:203], v[50:53]
	v_mfma_f32_16x16x32_bf16 v[42:45], v[180:183], v[208:211], v[42:45]
	v_mfma_f32_16x16x32_bf16 v[34:37], v[188:191], v[208:211], v[34:37]
	v_mfma_f32_16x16x32_bf16 v[30:33], v[180:183], v[232:235], v[30:33]
	v_mfma_f32_16x16x32_bf16 v[26:29], v[188:191], v[232:235], v[26:29]
	v_mfma_f32_16x16x32_bf16 v[14:17], v[180:183], v[240:243], v[14:17]
	v_mfma_f32_16x16x32_bf16 v[10:13], v[188:191], v[240:243], v[10:13]
	v_mfma_f32_16x16x32_bf16 v[58:61], v[184:187], v[204:207], v[58:61]
	v_mfma_f32_16x16x32_bf16 v[50:53], v[196:199], v[204:207], v[50:53]
	v_mfma_f32_16x16x32_bf16 v[42:45], v[184:187], v[228:231], v[42:45]
	v_mfma_f32_16x16x32_bf16 v[34:37], v[196:199], v[228:231], v[34:37]
	v_mfma_f32_16x16x32_bf16 v[30:33], v[184:187], v[236:239], v[30:33]
	v_mfma_f32_16x16x32_bf16 v[26:29], v[196:199], v[236:239], v[26:29]
	v_mfma_f32_16x16x32_bf16 v[14:17], v[184:187], v[244:247], v[14:17]
	v_mfma_f32_16x16x32_bf16 v[10:13], v[196:199], v[244:247], v[10:13]
	s_barrier
	s_add_i32 s74, s74, 2
	s_add_u32 s44, s44, 0x100
	s_addc_u32 s45, s45, 0
	s_cmp_gt_u32 s74, 29
	s_cbranch_scc1 .LBB0_1669

; #define PG8_AOFF(of, u) do { _Pragma("unroll") for (int hh_ = 0; hh_ < 2; ++hh_) _Pragma("unroll") for (int i_ = 0; i_ < 2; ++i_) { \
;         if constexpr (GATHER) of[hh_][i_] = (unsigned)gidx[(u).pm * 256 + hh_ * 128 + RA[i_]] * (unsigned)(lda * 2) + CA2[i_]; \
;         else of[hh_][i_] = (unsigned)((hh_ * HALF + RA[i_]) * lda) * 2u + CA2[i_]; } } while (0)
; #define PG8_STAGE(bufoff, gbase, voff) do { _Pragma("unroll") for (int _i = 0; _i < 2; ++_i) \
;         __builtin_amdgcn_global_load_lds((const unsigned*)((const char*)(gbase) + (voff)[_i]), (LAS unsigned*)(lds + (bufoff) + ldsw + _i * 8192), 16, 0, 0); } while (0)
; #define PG8_LDA(dst, b, h) do { _Pragma("unroll") for (int m = 0; m < 4; ++m) _Pragma("unroll") for (int k = 0; k < 2; ++k) dst[m][k] = *(const LAS bf16x8*)(lds + PG8_SA(b, h) + aoff + m * 2048 + k * 1024); } while (0)
; #define PG8_WAIT_V(n) asm volatile("s_waitcnt vmcnt(" #n ")" ::: "memory")
; #define PG8_WAIT_L(n) asm volatile("s_waitcnt lgkmcnt(" #n ")" ::: "memory")
; template <class Epi, class Sched, bool GATHER = false>
; __device__ __forceinline__ void gemm_phase(LAS unsigned char* lds, const int lda, const int ldb, const int K, const Sched& S, const Epi& E, const int* gidx = nullptr) {
;     ...
;             const bool last = (t == nt - 2);
;             if constexpr (GATHER) { if (last && has_next) PG8_AOFF(ofn, nxt); }
;             const char* a1 = cA + (size_t)(t + 1) * kstep;
;             const char* a2 = last ? nA : cA + (size_t)(t + 2) * kstep; const char* b2 = last ? nB : cB + (size_t)(t + 2) * kstep;
;             const char* a3 = a2 + kstep; const char* b3 = b2 + kstep;
;             unsigned o2[2][2];
; #pragma unroll
;             for (int hh = 0; hh < 2; ++hh)
; #pragma unroll
;                 for (int i = 0; i < 2; ++i) { if constexpr (GATHER) o2[hh][i] = last ? ofn[hh][i] : ofc[hh][i]; else o2[hh][i] = ofc[hh][i]; }
;             PG8_LDB(B0, 0, 0); PG8_LDB(B1, 0, 1); PG8_SCHED; PG8_LDA(At, 0, 0); PG8_STAGE(PG8_SA(1, 1), a1, ofc[1]);
;             PG8_WAIT_V(8); PG8_WAIT_L(0); PG8_BAR; PG8_MMA(0, 0, At, B0); PG8_MMA(0, 1, At, B1); PG8_BAR; PG8_SCHED;
;             PG8_LDA(At, 0, 1); PG8_STAGE(PG8_SB(0, 0), b2, voffB); PG8_STAGE(PG8_SB(0, 1), b2 + hstepB, voffB); PG8_STAGE(PG8_SA(0, 0), a2, o2[0]);
;             PG8_WAIT_V(8); PG8_WAIT_L(0); PG8_BAR; PG8_MMA(1, 0, At, B0); PG8_MMA(1, 1, At, B1); PG8_BAR; PG8_SCHED;
.LBB0_1733:
	s_add_i32 s28, 0, 0x10000
	v_add_u32_e32 v146, s28, v147
	s_add_i32 s33, 0, 0x14000
	ds_read_b128 v[152:155], v146
	ds_read_b128 v[156:159], v146 offset:1024
	ds_read_b128 v[160:163], v146 offset:2048
	ds_read_b128 v[164:167], v146 offset:3072
	v_add_u32_e32 v146, s33, v147
	ds_read_b128 v[168:171], v146
	ds_read_b128 v[172:175], v146 offset:1024
	ds_read_b128 v[176:179], v146 offset:2048
	ds_read_b128 v[180:183], v146 offset:3072
	ds_read_b128 v[184:187], v151
	ds_read_b128 v[188:191], v151 offset:1024
	ds_read_b128 v[196:199], v151 offset:2048
	ds_read_b128 v[200:203], v151 offset:3072
	ds_read_b128 v[204:207], v151 offset:4096
	ds_read_b128 v[208:211], v151 offset:5120
	ds_read_b128 v[228:231], v151 offset:6144
	ds_read_b128 v[232:235], v151 offset:7168
	v_lshl_add_u64 v[148:149], s[44:45], 0, v[144:145]
	s_add_i32 m0, s10, 0xc000
	s_add_u32 s12, s44, 0x80
	s_addc_u32 s13, s45, 0
	s_cmp_eq_u32 s72, 12
	s_cselect_b32 s49, s39, s13
	s_cselect_b32 s48, s38, s12
	s_cselect_b32 s13, s41, s71
	s_cselect_b32 s12, s40, s70
	global_load_lds_dwordx4 v[148:149], off
	v_lshl_add_u64 v[148:149], s[44:45], 0, v[142:143]
	s_add_i32 m0, s10, 0xe000
	s_nop 0
	global_load_lds_dwordx4 v[148:149], off
	s_waitcnt vmcnt(8)
	s_waitcnt lgkmcnt(0)
	s_barrier
	v_mfma_f32_16x16x32_bf16 v[126:129], v[152:155], v[184:187], v[126:129]
	v_mfma_f32_16x16x32_bf16 v[122:125], v[160:163], v[184:187], v[122:125]
	v_mfma_f32_16x16x32_bf16 v[110:113], v[152:155], v[196:199], v[110:113]
	v_mfma_f32_16x16x32_bf16 v[106:109], v[160:163], v[196:199], v[106:109]
	v_mfma_f32_16x16x32_bf16 v[94:97], v[152:155], v[204:207], v[94:97]
	v_mfma_f32_16x16x32_bf16 v[90:93], v[160:163], v[204:207], v[90:93]
	v_mfma_f32_16x16x32_bf16 v[82:85], v[152:155], v[228:231], v[82:85]
	v_mfma_f32_16x16x32_bf16 v[74:77], v[160:163], v[228:231], v[74:77]
	v_mfma_f32_16x16x32_bf16 v[126:129], v[156:159], v[188:191], v[126:129]
	v_mfma_f32_16x16x32_bf16 v[122:125], v[164:167], v[188:191], v[122:125]
	v_mfma_f32_16x16x32_bf16 v[110:113], v[156:159], v[200:203], v[110:113]
	v_mfma_f32_16x16x32_bf16 v[106:109], v[164:167], v[200:203], v[106:109]
	v_mfma_f32_16x16x32_bf16 v[94:97], v[156:159], v[208:211], v[94:97]
	v_mfma_f32_16x16x32_bf16 v[90:93], v[164:167], v[208:211], v[90:93]
	v_mfma_f32_16x16x32_bf16 v[82:85], v[156:159], v[232:235], v[82:85]
	v_mfma_f32_16x16x32_bf16 v[74:77], v[164:167], v[232:235], v[74:77]
	v_mfma_f32_16x16x32_bf16 v[118:121], v[168:171], v[184:187], v[118:121]
	v_mfma_f32_16x16x32_bf16 v[114:117], v[176:179], v[184:187], v[114:117]
	v_mfma_f32_16x16x32_bf16 v[102:105], v[168:171], v[196:199], v[102:105]
	v_mfma_f32_16x16x32_bf16 v[98:101], v[176:179], v[196:199], v[98:101]
	v_mfma_f32_16x16x32_bf16 v[86:89], v[168:171], v[204:207], v[86:89]
	v_mfma_f32_16x16x32_bf16 v[78:81], v[176:179], v[204:207], v[78:81]
	v_mfma_f32_16x16x32_bf16 v[62:65], v[168:171], v[228:231], v[62:65]
	v_mfma_f32_16x16x32_bf16 v[58:61], v[176:179], v[228:231], v[58:61]
	v_mfma_f32_16x16x32_bf16 v[118:121], v[172:175], v[188:191], v[118:121]
	v_mfma_f32_16x16x32_bf16 v[114:117], v[180:183], v[188:191], v[114:117]
	v_mfma_f32_16x16x32_bf16 v[102:105], v[172:175], v[200:203], v[102:105]
	v_mfma_f32_16x16x32_bf16 v[98:101], v[180:183], v[200:203], v[98:101]
	v_mfma_f32_16x16x32_bf16 v[86:89], v[172:175], v[208:211], v[86:89]
	v_mfma_f32_16x16x32_bf16 v[78:81], v[180:183], v[208:211], v[78:81]
	v_mfma_f32_16x16x32_bf16 v[62:65], v[172:175], v[232:235], v[62:65]
	v_mfma_f32_16x16x32_bf16 v[58:61], v[180:183], v[232:235], v[58:61]
	s_barrier
	ds_read_b128 v[184:187], v151 offset:16384
	ds_read_b128 v[188:191], v151 offset:17408
	ds_read_b128 v[196:199], v151 offset:18432
	ds_read_b128 v[200:203], v151 offset:19456
	ds_read_b128 v[204:207], v151 offset:20480
	ds_read_b128 v[208:211], v151 offset:21504
	ds_read_b128 v[228:231], v151 offset:22528
	ds_read_b128 v[232:235], v151 offset:23552
	s_add_i32 s28, s28, s9
	v_lshl_add_u64 v[148:149], s[12:13], 0, v[132:133]
	s_mov_b32 m0, s28
	s_nop 0
	global_load_lds_dwordx4 v[148:149], off
	s_add_i32 m0, s28, 0x2000
	s_add_u32 s28, s12, 0x40000
	v_lshl_add_u64 v[192:193], s[12:13], 0, v[130:131]
	s_addc_u32 s29, s13, 0
	s_add_i32 s33, s33, s9
	global_load_lds_dwordx4 v[192:193], off
	v_lshl_add_u64 v[214:215], s[28:29], 0, v[132:133]
	s_mov_b32 m0, s33
	v_lshl_add_u64 v[222:223], s[48:49], 0, v[136:137]
	global_load_lds_dwordx4 v[214:215], off
	v_lshl_add_u64 v[214:215], s[28:29], 0, v[130:131]
	s_add_i32 m0, s33, 0x2000
	s_nop 0
	global_load_lds_dwordx4 v[214:215], off
	v_lshl_add_u64 v[214:215], s[48:49], 0, v[134:135]
	s_mov_b32 m0, s10
	s_nop 0
	global_load_lds_dwordx4 v[214:215], off
	s_mov_b32 m0, s11
	s_nop 0
	global_load_lds_dwordx4 v[222:223], off
	s_waitcnt vmcnt(8)
	s_waitcnt lgkmcnt(0)
	s_barrier
; #define PG8_STAGE(bufoff, gbase, voff) do { _Pragma("unroll") for (int _i = 0; _i < 2; ++_i) \
;         __builtin_amdgcn_global_load_lds((const unsigned*)((const char*)(gbase) + (voff)[_i]), (LAS unsigned*)(lds + (bufoff) + ldsw + _i * 8192), 16, 0, 0); } while (0)
; #define PG8_LDA(dst, b, h) do { _Pragma("unroll") for (int m = 0; m < 4; ++m) _Pragma("unroll") for (int k = 0; k < 2; ++k) dst[m][k] = *(const LAS bf16x8*)(lds + PG8_SA(b, h) + aoff + m * 2048 + k * 1024); } while (0)
; #define PG8_LDB(dst, b, h) do { _Pragma("unroll") for (int n = 0; n < 2; ++n) _Pragma("unroll") for (int k = 0; k < 2; ++k) dst[n][k] = *(const LAS bf16x8*)(lds + PG8_SB(b, h) + boff + n * 2048 + k * 1024); } while (0)
; #define PG8_MMA(ai, bj, At, Bt) do { __builtin_amdgcn_s_setprio(1); _Pragma("unroll") for (int m = 0; m < 4; ++m) _Pragma("unroll") for (int n = 0; n < 2; ++n) _Pragma("unroll") for (int k = 0; k < 2; ++k) \
;         acc[ai][bj][m][n] = __builtin_amdgcn_mfma_f32_16x16x32_bf16(Bt[n][k], At[m][k], acc[ai][bj][m][n], 0, 0, 0); __builtin_amdgcn_s_setprio(0); } while (0)
; #define PG8_WAIT_V(n) asm volatile("s_waitcnt vmcnt(" #n ")" ::: "memory")
; #define PG8_WAIT_L(n) asm volatile("s_waitcnt lgkmcnt(" #n ")" ::: "memory")
; #define PG8_BAR __builtin_amdgcn_s_barrier()
; #define PG8_SCHED __builtin_amdgcn_sched_barrier(0)
; template <class Epi, class Sched, bool GATHER = false>
; __device__ __forceinline__ void gemm_phase(LAS unsigned char* lds, const int lda, const int ldb, const int K, const Sched& S, const Epi& E, const int* gidx = nullptr) {
;     ...
;             PG8_WAIT_V(8); PG8_WAIT_L(0); PG8_BAR; PG8_MMA(1, 0, At, B0); PG8_MMA(1, 1, At, B1); PG8_BAR; PG8_SCHED;
;             PG8_LDB(B0, 1, 0); PG8_LDB(B1, 1, 1); PG8_SCHED; PG8_LDA(At, 1, 0); PG8_STAGE(PG8_SA(0, 1), a2, o2[1]);
;             PG8_WAIT_V(8); PG8_WAIT_L(0); PG8_BAR; PG8_MMA(0, 0, At, B0); PG8_MMA(0, 1, At, B1); PG8_BAR; PG8_SCHED;
	v_mfma_f32_16x16x32_bf16 v[54:57], v[152:155], v[184:187], v[54:57]
	v_mfma_f32_16x16x32_bf16 v[50:53], v[160:163], v[184:187], v[50:53]
	v_mfma_f32_16x16x32_bf16 v[30:33], v[152:155], v[196:199], v[30:33]
	v_mfma_f32_16x16x32_bf16 v[26:29], v[160:163], v[196:199], v[26:29]
	v_mfma_f32_16x16x32_bf16 v[14:17], v[152:155], v[204:207], v[14:17]
	v_mfma_f32_16x16x32_bf16 v[10:13], v[160:163], v[204:207], v[10:13]
	v_mfma_f32_16x16x32_bf16 v[6:9], v[152:155], v[228:231], v[6:9]
	v_mfma_f32_16x16x32_bf16 v[2:5], v[160:163], v[228:231], v[2:5]
	v_mfma_f32_16x16x32_bf16 v[54:57], v[156:159], v[188:191], v[54:57]
	v_mfma_f32_16x16x32_bf16 v[50:53], v[164:167], v[188:191], v[50:53]
	v_mfma_f32_16x16x32_bf16 v[30:33], v[156:159], v[200:203], v[30:33]
	v_mfma_f32_16x16x32_bf16 v[26:29], v[164:167], v[200:203], v[26:29]
	v_mfma_f32_16x16x32_bf16 v[14:17], v[156:159], v[208:211], v[14:17]
	v_mfma_f32_16x16x32_bf16 v[10:13], v[164:167], v[208:211], v[10:13]
	v_mfma_f32_16x16x32_bf16 v[6:9], v[156:159], v[232:235], v[6:9]
	v_mfma_f32_16x16x32_bf16 v[2:5], v[164:167], v[232:235], v[2:5]
	v_mfma_f32_16x16x32_bf16 v[66:69], v[168:171], v[184:187], v[66:69]
	v_mfma_f32_16x16x32_bf16 v[70:73], v[176:179], v[184:187], v[70:73]
	v_mfma_f32_16x16x32_bf16 v[42:45], v[168:171], v[196:199], v[42:45]
	v_mfma_f32_16x16x32_bf16 v[46:49], v[176:179], v[196:199], v[46:49]
	v_mfma_f32_16x16x32_bf16 v[34:37], v[168:171], v[204:207], v[34:37]
	v_mfma_f32_16x16x32_bf16 v[38:41], v[176:179], v[204:207], v[38:41]
	v_mfma_f32_16x16x32_bf16 v[18:21], v[168:171], v[228:231], v[18:21]
	v_mfma_f32_16x16x32_bf16 v[22:25], v[176:179], v[228:231], v[22:25]
	v_mfma_f32_16x16x32_bf16 v[66:69], v[172:175], v[188:191], v[66:69]
	v_mfma_f32_16x16x32_bf16 v[70:73], v[180:183], v[188:191], v[70:73]
	v_mfma_f32_16x16x32_bf16 v[42:45], v[172:175], v[200:203], v[42:45]
	v_mfma_f32_16x16x32_bf16 v[46:49], v[180:183], v[200:203], v[46:49]
	v_mfma_f32_16x16x32_bf16 v[34:37], v[172:175], v[208:211], v[34:37]
	v_mfma_f32_16x16x32_bf16 v[38:41], v[180:183], v[208:211], v[38:41]
	v_mfma_f32_16x16x32_bf16 v[18:21], v[172:175], v[232:235], v[18:21]
	v_mfma_f32_16x16x32_bf16 v[22:25], v[180:183], v[232:235], v[22:25]
	s_barrier
	s_add_i32 s28, 0, 0x18000
	v_add_u32_e32 v146, s28, v147
	s_add_i32 s29, 0, 0x1c000
	ds_read_b128 v[152:155], v146
	ds_read_b128 v[156:159], v146 offset:1024
	ds_read_b128 v[160:163], v146 offset:2048
	ds_read_b128 v[164:167], v146 offset:3072
	v_add_u32_e32 v146, s29, v147
	ds_read_b128 v[168:171], v146
	ds_read_b128 v[172:175], v146 offset:1024
	ds_read_b128 v[176:179], v146 offset:2048
	ds_read_b128 v[180:183], v146 offset:3072
	ds_read_b128 v[184:187], v151 offset:32768
	ds_read_b128 v[188:191], v151 offset:33792
	ds_read_b128 v[196:199], v151 offset:34816
	ds_read_b128 v[200:203], v151 offset:35840
	ds_read_b128 v[204:207], v151 offset:36864
	ds_read_b128 v[208:211], v151 offset:37888
	ds_read_b128 v[228:231], v151 offset:38912
	ds_read_b128 v[232:235], v151 offset:39936
	s_mov_b32 m0, s22
	v_lshl_add_u64 v[224:225], s[48:49], 0, v[138:139]
	global_load_lds_dwordx4 v[224:225], off
	v_lshl_add_u64 v[224:225], s[48:49], 0, v[140:141]
	s_mov_b32 m0, s23
	s_nop 0
	global_load_lds_dwordx4 v[224:225], off
	s_waitcnt vmcnt(8)
	s_waitcnt lgkmcnt(0)
	s_barrier
	v_mfma_f32_16x16x32_bf16 v[126:129], v[152:155], v[184:187], v[126:129]
	v_mfma_f32_16x16x32_bf16 v[122:125], v[160:163], v[184:187], v[122:125]
	v_mfma_f32_16x16x32_bf16 v[110:113], v[152:155], v[196:199], v[110:113]
	v_mfma_f32_16x16x32_bf16 v[106:109], v[160:163], v[196:199], v[106:109]
	v_mfma_f32_16x16x32_bf16 v[94:97], v[152:155], v[204:207], v[94:97]
	v_mfma_f32_16x16x32_bf16 v[90:93], v[160:163], v[204:207], v[90:93]
	v_mfma_f32_16x16x32_bf16 v[82:85], v[152:155], v[228:231], v[82:85]
	v_mfma_f32_16x16x32_bf16 v[74:77], v[160:163], v[228:231], v[74:77]
	v_mfma_f32_16x16x32_bf16 v[126:129], v[156:159], v[188:191], v[126:129]
	v_mfma_f32_16x16x32_bf16 v[122:125], v[164:167], v[188:191], v[122:125]
	v_mfma_f32_16x16x32_bf16 v[110:113], v[156:159], v[200:203], v[110:113]
	v_mfma_f32_16x16x32_bf16 v[106:109], v[164:167], v[200:203], v[106:109]
	v_mfma_f32_16x16x32_bf16 v[94:97], v[156:159], v[208:211], v[94:97]
	v_mfma_f32_16x16x32_bf16 v[90:93], v[164:167], v[208:211], v[90:93]
	v_mfma_f32_16x16x32_bf16 v[82:85], v[156:159], v[232:235], v[82:85]
	v_mfma_f32_16x16x32_bf16 v[74:77], v[164:167], v[232:235], v[74:77]
	v_mfma_f32_16x16x32_bf16 v[118:121], v[168:171], v[184:187], v[118:121]
	v_mfma_f32_16x16x32_bf16 v[114:117], v[176:179], v[184:187], v[114:117]
	v_mfma_f32_16x16x32_bf16 v[102:105], v[168:171], v[196:199], v[102:105]
	v_mfma_f32_16x16x32_bf16 v[98:101], v[176:179], v[196:199], v[98:101]
	v_mfma_f32_16x16x32_bf16 v[86:89], v[168:171], v[204:207], v[86:89]
	v_mfma_f32_16x16x32_bf16 v[78:81], v[176:179], v[204:207], v[78:81]
	v_mfma_f32_16x16x32_bf16 v[62:65], v[168:171], v[228:231], v[62:65]
	v_mfma_f32_16x16x32_bf16 v[58:61], v[176:179], v[228:231], v[58:61]
	v_mfma_f32_16x16x32_bf16 v[118:121], v[172:175], v[188:191], v[118:121]
	v_mfma_f32_16x16x32_bf16 v[114:117], v[180:183], v[188:191], v[114:117]
	v_mfma_f32_16x16x32_bf16 v[102:105], v[172:175], v[200:203], v[102:105]
	v_mfma_f32_16x16x32_bf16 v[98:101], v[180:183], v[200:203], v[98:101]
	v_mfma_f32_16x16x32_bf16 v[86:89], v[172:175], v[208:211], v[86:89]
	v_mfma_f32_16x16x32_bf16 v[78:81], v[180:183], v[208:211], v[78:81]
	v_mfma_f32_16x16x32_bf16 v[62:65], v[172:175], v[232:235], v[62:65]
	v_mfma_f32_16x16x32_bf16 v[58:61], v[180:183], v[232:235], v[58:61]
	s_barrier
; #define PG8_STAGE(bufoff, gbase, voff) do { _Pragma("unroll") for (int _i = 0; _i < 2; ++_i) \
;         __builtin_amdgcn_global_load_lds((const unsigned*)((const char*)(gbase) + (voff)[_i]), (LAS unsigned*)(lds + (bufoff) + ldsw + _i * 8192), 16, 0, 0); } while (0)
; #define PG8_LDA(dst, b, h) do { _Pragma("unroll") for (int m = 0; m < 4; ++m) _Pragma("unroll") for (int k = 0; k < 2; ++k) dst[m][k] = *(const LAS bf16x8*)(lds + PG8_SA(b, h) + aoff + m * 2048 + k * 1024); } while (0)
; #define PG8_MMA(ai, bj, At, Bt) do { __builtin_amdgcn_s_setprio(1); _Pragma("unroll") for (int m = 0; m < 4; ++m) _Pragma("unroll") for (int n = 0; n < 2; ++n) _Pragma("unroll") for (int k = 0; k < 2; ++k) \
;         acc[ai][bj][m][n] = __builtin_amdgcn_mfma_f32_16x16x32_bf16(Bt[n][k], At[m][k], acc[ai][bj][m][n], 0, 0, 0); __builtin_amdgcn_s_setprio(0); } while (0)
; #define PG8_WAIT_V(n) asm volatile("s_waitcnt vmcnt(" #n ")" ::: "memory")
; #define PG8_WAIT_L(n) asm volatile("s_waitcnt lgkmcnt(" #n ")" ::: "memory")
; #define PG8_BAR __builtin_amdgcn_s_barrier()
; #define PG8_SCHED __builtin_amdgcn_sched_barrier(0)
; template <class Epi, class Sched, bool GATHER = false>
; __device__ __forceinline__ void gemm_phase(LAS unsigned char* lds, const int lda, const int ldb, const int K, const Sched& S, const Epi& E, const int* gidx = nullptr) {
;     ...
;             PG8_LDA(At, 1, 1); PG8_STAGE(PG8_SB(1, 0), b3, voffB); PG8_STAGE(PG8_SB(1, 1), b3 + hstepB, voffB); PG8_STAGE(PG8_SA(1, 0), a3, o2[0]);
;             PG8_WAIT_V(8); PG8_WAIT_L(0); PG8_BAR; PG8_MMA(1, 0, At, B0); PG8_MMA(1, 1, At, B1); PG8_BAR; PG8_SCHED;
;         }
;         if (wr == 0) PG8_BAR;
	ds_read_b128 v[184:187], v151 offset:49152
	ds_read_b128 v[188:191], v151 offset:50176
	ds_read_b128 v[196:199], v151 offset:51200
	ds_read_b128 v[200:203], v151 offset:52224
	ds_read_b128 v[204:207], v151 offset:53248
	ds_read_b128 v[208:211], v151 offset:54272
	ds_read_b128 v[228:231], v151 offset:55296
	ds_read_b128 v[232:235], v151 offset:56320
	s_add_i32 s28, s28, s9
	v_lshl_add_u64 v[148:149], v[148:149], 0, s[64:65]
	s_mov_b32 m0, s28
	s_nop 0
	global_load_lds_dwordx4 v[148:149], off
	s_add_i32 m0, s28, 0x2000
	s_add_u32 s12, s12, 0x40080
	v_lshl_add_u64 v[148:149], v[192:193], 0, s[64:65]
	s_addc_u32 s13, s13, 0
	s_add_i32 s28, s29, s9
	global_load_lds_dwordx4 v[148:149], off
	v_lshl_add_u64 v[148:149], s[12:13], 0, v[132:133]
	s_mov_b32 m0, s28
	s_nop 0
	global_load_lds_dwordx4 v[148:149], off
	v_lshl_add_u64 v[148:149], s[12:13], 0, v[130:131]
	s_add_i32 m0, s28, 0x2000
	s_nop 0
	global_load_lds_dwordx4 v[148:149], off
	v_lshl_add_u64 v[148:149], v[214:215], 0, s[64:65]
	s_mov_b32 m0, s50
	s_nop 0
	global_load_lds_dwordx4 v[148:149], off
	v_lshl_add_u64 v[148:149], v[222:223], 0, s[64:65]
	s_mov_b32 m0, s51
	s_nop 0
	global_load_lds_dwordx4 v[148:149], off
	s_waitcnt vmcnt(8)
	s_waitcnt lgkmcnt(0)
	s_barrier
	v_mfma_f32_16x16x32_bf16 v[54:57], v[152:155], v[184:187], v[54:57]
	v_mfma_f32_16x16x32_bf16 v[50:53], v[160:163], v[184:187], v[50:53]
	v_mfma_f32_16x16x32_bf16 v[30:33], v[152:155], v[196:199], v[30:33]
	v_mfma_f32_16x16x32_bf16 v[26:29], v[160:163], v[196:199], v[26:29]
	v_mfma_f32_16x16x32_bf16 v[14:17], v[152:155], v[204:207], v[14:17]
	v_mfma_f32_16x16x32_bf16 v[10:13], v[160:163], v[204:207], v[10:13]
	v_mfma_f32_16x16x32_bf16 v[6:9], v[152:155], v[228:231], v[6:9]
	v_mfma_f32_16x16x32_bf16 v[2:5], v[160:163], v[228:231], v[2:5]
	v_mfma_f32_16x16x32_bf16 v[54:57], v[156:159], v[188:191], v[54:57]
	v_mfma_f32_16x16x32_bf16 v[50:53], v[164:167], v[188:191], v[50:53]
	v_mfma_f32_16x16x32_bf16 v[30:33], v[156:159], v[200:203], v[30:33]
	v_mfma_f32_16x16x32_bf16 v[26:29], v[164:167], v[200:203], v[26:29]
	v_mfma_f32_16x16x32_bf16 v[14:17], v[156:159], v[208:211], v[14:17]
	v_mfma_f32_16x16x32_bf16 v[10:13], v[164:167], v[208:211], v[10:13]
	v_mfma_f32_16x16x32_bf16 v[6:9], v[156:159], v[232:235], v[6:9]
	v_mfma_f32_16x16x32_bf16 v[2:5], v[164:167], v[232:235], v[2:5]
	v_mfma_f32_16x16x32_bf16 v[66:69], v[168:171], v[184:187], v[66:69]
	v_mfma_f32_16x16x32_bf16 v[70:73], v[176:179], v[184:187], v[70:73]
	v_mfma_f32_16x16x32_bf16 v[42:45], v[168:171], v[196:199], v[42:45]
	v_mfma_f32_16x16x32_bf16 v[46:49], v[176:179], v[196:199], v[46:49]
	v_mfma_f32_16x16x32_bf16 v[34:37], v[168:171], v[204:207], v[34:37]
	v_mfma_f32_16x16x32_bf16 v[38:41], v[176:179], v[204:207], v[38:41]
	v_mfma_f32_16x16x32_bf16 v[18:21], v[168:171], v[228:231], v[18:21]
	v_mfma_f32_16x16x32_bf16 v[22:25], v[176:179], v[228:231], v[22:25]
	v_mfma_f32_16x16x32_bf16 v[66:69], v[172:175], v[188:191], v[66:69]
	v_mfma_f32_16x16x32_bf16 v[70:73], v[180:183], v[188:191], v[70:73]
	v_mfma_f32_16x16x32_bf16 v[42:45], v[172:175], v[200:203], v[42:45]
	v_mfma_f32_16x16x32_bf16 v[46:49], v[180:183], v[200:203], v[46:49]
	v_mfma_f32_16x16x32_bf16 v[34:37], v[172:175], v[208:211], v[34:37]
	v_mfma_f32_16x16x32_bf16 v[38:41], v[180:183], v[208:211], v[38:41]
	v_mfma_f32_16x16x32_bf16 v[18:21], v[172:175], v[232:235], v[18:21]
	v_mfma_f32_16x16x32_bf16 v[22:25], v[180:183], v[232:235], v[22:25]
	s_barrier
	s_add_i32 s72, s72, 2
	s_add_u32 s44, s44, 0x100
	s_addc_u32 s45, s45, 0
	s_add_u32 s70, s70, 0x100
	s_addc_u32 s71, s71, 0
	s_cmp_gt_u32 s72, 13
	s_cbranch_scc0 .LBB0_1733
	s_and_b64 vcc, exec, s[36:37]
	s_cbranch_vccz .LBB0_1736
	s_barrier
